# added: LRU fix-up step pipelined, GEMM EpiStoreBf16 row-scale loads hoisted (one wait per tile), redundant vmcnt(0) drains removed at GEMM tile starts and before the router K loop, phase-1 barrier ski
# speedup vs baseline: 1.0077x; 1.0077x over previous
.LBB0_138:
	s_branch .LBB0_189

.LBB0_271:
	s_xor_b64 s[16:17], s[26:27], -1
	s_add_u32 s12, s42, s8
	s_addc_u32 s13, s43, s9
	s_and_b64 s[2:3], s[26:27], exec
	s_cselect_b32 s19, s13, s23
	s_cselect_b32 s85, s12, s22
	s_add_u32 s14, s46, s10
	s_addc_u32 s15, s47, s11
	s_and_b64 s[2:3], s[26:27], exec
	s_cselect_b32 vcc_lo, s15, s25
	s_cselect_b32 vcc_hi, s14, s24
	s_add_u32 s22, s22, 0x80080
	s_addc_u32 s23, s23, 0
	s_add_u32 s2, s24, 0x100
	v_mov_b32_e32 v0, 0
	s_addc_u32 s3, s25, 0
	s_mov_b32 s64, -2
	v_mov_b32_e32 v1, v0
	v_mov_b32_e32 v2, v0
	v_mov_b32_e32 v3, v0
	v_mov_b32_e32 v4, v0
	v_mov_b32_e32 v5, v0
	v_mov_b32_e32 v6, v0
	v_mov_b32_e32 v7, v0
	v_mov_b32_e32 v16, v0
	v_mov_b32_e32 v17, v0
	v_mov_b32_e32 v18, v0
	v_mov_b32_e32 v19, v0
	v_mov_b32_e32 v20, v0
	v_mov_b32_e32 v21, v0
	v_mov_b32_e32 v22, v0
	v_mov_b32_e32 v23, v0
	v_mov_b32_e32 v32, v0
	v_mov_b32_e32 v33, v0
	v_mov_b32_e32 v34, v0
	v_mov_b32_e32 v35, v0
	v_mov_b32_e32 v36, v0
	v_mov_b32_e32 v37, v0
	v_mov_b32_e32 v38, v0
	v_mov_b32_e32 v39, v0
	v_mov_b32_e32 v48, v0
	v_mov_b32_e32 v49, v0
	v_mov_b32_e32 v50, v0
	v_mov_b32_e32 v51, v0
	v_mov_b32_e32 v52, v0
	v_mov_b32_e32 v53, v0
	v_mov_b32_e32 v54, v0
	v_mov_b32_e32 v55, v0
	v_mov_b32_e32 v8, v0
	v_mov_b32_e32 v9, v0
	v_mov_b32_e32 v10, v0
	v_mov_b32_e32 v11, v0
	v_mov_b32_e32 v12, v0
	v_mov_b32_e32 v13, v0
	v_mov_b32_e32 v14, v0
	v_mov_b32_e32 v15, v0
	v_mov_b32_e32 v24, v0
	v_mov_b32_e32 v25, v0
	v_mov_b32_e32 v26, v0
	v_mov_b32_e32 v27, v0
	v_mov_b32_e32 v28, v0
	v_mov_b32_e32 v29, v0
	v_mov_b32_e32 v30, v0
	v_mov_b32_e32 v31, v0
	v_mov_b32_e32 v40, v0
	v_mov_b32_e32 v41, v0
	v_mov_b32_e32 v42, v0
	v_mov_b32_e32 v43, v0
	v_mov_b32_e32 v44, v0
	v_mov_b32_e32 v45, v0
	v_mov_b32_e32 v46, v0
	v_mov_b32_e32 v47, v0
	v_mov_b32_e32 v56, v0
	v_mov_b32_e32 v57, v0
	v_mov_b32_e32 v58, v0
	v_mov_b32_e32 v59, v0
	v_mov_b32_e32 v60, v0
	v_mov_b32_e32 v61, v0
	v_mov_b32_e32 v62, v0
	v_mov_b32_e32 v63, v0
	v_mov_b32_e32 v64, v0
	v_mov_b32_e32 v65, v0
	v_mov_b32_e32 v66, v0
	v_mov_b32_e32 v67, v0
	v_mov_b32_e32 v68, v0
	v_mov_b32_e32 v69, v0
	v_mov_b32_e32 v70, v0
	v_mov_b32_e32 v71, v0
	v_mov_b32_e32 v80, v0
	v_mov_b32_e32 v81, v0
	v_mov_b32_e32 v82, v0
	v_mov_b32_e32 v83, v0
	v_mov_b32_e32 v84, v0
	v_mov_b32_e32 v85, v0
	v_mov_b32_e32 v86, v0
	v_mov_b32_e32 v87, v0
	v_mov_b32_e32 v96, v0
	v_mov_b32_e32 v97, v0
	v_mov_b32_e32 v98, v0
	v_mov_b32_e32 v99, v0
	v_mov_b32_e32 v100, v0
	v_mov_b32_e32 v101, v0
	v_mov_b32_e32 v102, v0
	v_mov_b32_e32 v103, v0
	v_mov_b32_e32 v112, v0
	v_mov_b32_e32 v113, v0
	v_mov_b32_e32 v114, v0
	v_mov_b32_e32 v115, v0
	v_mov_b32_e32 v116, v0
	v_mov_b32_e32 v117, v0
	v_mov_b32_e32 v118, v0
	v_mov_b32_e32 v119, v0
	v_mov_b32_e32 v72, v0
	v_mov_b32_e32 v73, v0
	v_mov_b32_e32 v74, v0
	v_mov_b32_e32 v75, v0
	v_mov_b32_e32 v76, v0
	v_mov_b32_e32 v77, v0
	v_mov_b32_e32 v78, v0
	v_mov_b32_e32 v79, v0
	v_mov_b32_e32 v88, v0
	v_mov_b32_e32 v89, v0
	v_mov_b32_e32 v90, v0
	v_mov_b32_e32 v91, v0
	v_mov_b32_e32 v92, v0
	v_mov_b32_e32 v93, v0
	v_mov_b32_e32 v94, v0
	v_mov_b32_e32 v95, v0
	v_mov_b32_e32 v104, v0
	v_mov_b32_e32 v105, v0
	v_mov_b32_e32 v106, v0
	v_mov_b32_e32 v107, v0
	v_mov_b32_e32 v108, v0
	v_mov_b32_e32 v109, v0
	v_mov_b32_e32 v110, v0
	v_mov_b32_e32 v111, v0
	v_mov_b32_e32 v120, v0
	v_mov_b32_e32 v121, v0
	v_mov_b32_e32 v122, v0
	v_mov_b32_e32 v123, v0
	v_mov_b32_e32 v124, v0
	v_mov_b32_e32 v125, v0
	v_mov_b32_e32 v126, v0
	v_mov_b32_e32 v127, v0
.LBB0_272:
	s_add_u32 s24, s22, 0xfff80080
	s_addc_u32 s25, s23, -1
	s_add_i32 s28, 0, 0x10000
	v_add_u32_e32 v136, s28, v139
	ds_read_b128 v[144:147], v136
	ds_read_b128 v[148:151], v136 offset:1024
	ds_read_b128 v[152:155], v136 offset:2048
	ds_read_b128 v[156:159], v136 offset:3072
	s_cmp_eq_u32 s64, 12
	s_cselect_b32 s27, s19, s25
	s_cselect_b32 s26, s85, s24
	s_cselect_b32 s25, vcc_lo, s3
	s_cselect_b32 s24, vcc_hi, s2
	v_lshl_add_u64 v[136:137], s[22:23], 0, v[132:133]
	s_add_i32 m0, s57, 0xc000
	ds_read_b128 v[160:163], v143
	ds_read_b128 v[164:167], v143 offset:1024
	ds_read_b128 v[168:171], v143 offset:2048
	ds_read_b128 v[172:175], v143 offset:3072
	ds_read_b128 v[176:179], v143 offset:4096
	ds_read_b128 v[180:183], v143 offset:5120
	ds_read_b128 v[184:187], v143 offset:6144
	ds_read_b128 v[188:191], v143 offset:7168
	global_load_lds_dwordx4 v[136:137], off
	v_lshl_add_u64 v[136:137], s[22:23], 0, v[134:135]
	s_add_i32 m0, s57, 0xe000
	s_nop 0
	global_load_lds_dwordx4 v[136:137], off
	s_waitcnt lgkmcnt(8)
	s_barrier
	s_waitcnt lgkmcnt(0)
	s_setprio 1
	s_waitcnt lgkmcnt(0)
	v_mfma_f32_16x16x32_bf16 v[124:127], v[144:147], v[160:163], v[124:127]
	v_mfma_f32_16x16x32_bf16 v[120:123], v[152:155], v[160:163], v[120:123]
	v_mfma_f32_16x16x32_bf16 v[108:111], v[144:147], v[168:171], v[108:111]
	v_mfma_f32_16x16x32_bf16 v[104:107], v[152:155], v[168:171], v[104:107]
	v_mfma_f32_16x16x32_bf16 v[92:95], v[144:147], v[176:179], v[92:95]
	v_mfma_f32_16x16x32_bf16 v[88:91], v[152:155], v[176:179], v[88:91]
	v_mfma_f32_16x16x32_bf16 v[76:79], v[144:147], v[184:187], v[76:79]
	v_mfma_f32_16x16x32_bf16 v[72:75], v[152:155], v[184:187], v[72:75]
	v_mfma_f32_16x16x32_bf16 v[124:127], v[148:151], v[164:167], v[124:127]
	v_mfma_f32_16x16x32_bf16 v[120:123], v[156:159], v[164:167], v[120:123]
	v_mfma_f32_16x16x32_bf16 v[108:111], v[148:151], v[172:175], v[108:111]
	v_mfma_f32_16x16x32_bf16 v[104:107], v[156:159], v[172:175], v[104:107]
	v_mfma_f32_16x16x32_bf16 v[92:95], v[148:151], v[180:183], v[92:95]
	v_mfma_f32_16x16x32_bf16 v[88:91], v[156:159], v[180:183], v[88:91]
	v_mfma_f32_16x16x32_bf16 v[76:79], v[148:151], v[188:191], v[76:79]
	v_mfma_f32_16x16x32_bf16 v[72:75], v[156:159], v[188:191], v[72:75]
	s_setprio 0
	s_barrier
	s_add_i32 s65, 0, 0x14000
	v_add_u32_e32 v136, s65, v139
	s_add_i32 s28, s28, s56
	ds_read_b128 v[192:195], v136
	ds_read_b128 v[196:199], v136 offset:1024
	ds_read_b128 v[200:203], v136 offset:2048
	ds_read_b128 v[204:207], v136 offset:3072
	v_lshl_add_u64 v[136:137], s[24:25], 0, v[128:129]
	s_mov_b32 m0, s28
	v_lshl_add_u64 v[212:213], s[24:25], 0, v[130:131]
	global_load_lds_dwordx4 v[136:137], off
	s_add_i32 m0, s28, 0x2000
	s_nop 0
	global_load_lds_dwordx4 v[212:213], off
	s_barrier
	s_waitcnt lgkmcnt(0)
	s_setprio 1
	s_waitcnt lgkmcnt(0)
	v_mfma_f32_16x16x32_bf16 v[116:119], v[192:195], v[160:163], v[116:119]
	v_mfma_f32_16x16x32_bf16 v[112:115], v[200:203], v[160:163], v[112:115]
	v_mfma_f32_16x16x32_bf16 v[100:103], v[192:195], v[168:171], v[100:103]
	v_mfma_f32_16x16x32_bf16 v[96:99], v[200:203], v[168:171], v[96:99]
	v_mfma_f32_16x16x32_bf16 v[84:87], v[192:195], v[176:179], v[84:87]
	v_mfma_f32_16x16x32_bf16 v[80:83], v[200:203], v[176:179], v[80:83]
	v_mfma_f32_16x16x32_bf16 v[68:71], v[192:195], v[184:187], v[68:71]
	v_mfma_f32_16x16x32_bf16 v[64:67], v[200:203], v[184:187], v[64:67]
	v_mfma_f32_16x16x32_bf16 v[116:119], v[196:199], v[164:167], v[116:119]
	v_mfma_f32_16x16x32_bf16 v[112:115], v[204:207], v[164:167], v[112:115]
	v_mfma_f32_16x16x32_bf16 v[100:103], v[196:199], v[172:175], v[100:103]
	v_mfma_f32_16x16x32_bf16 v[96:99], v[204:207], v[172:175], v[96:99]
	v_mfma_f32_16x16x32_bf16 v[84:87], v[196:199], v[180:183], v[84:87]
	v_mfma_f32_16x16x32_bf16 v[80:83], v[204:207], v[180:183], v[80:83]
	v_mfma_f32_16x16x32_bf16 v[68:71], v[196:199], v[188:191], v[68:71]
	v_mfma_f32_16x16x32_bf16 v[64:67], v[204:207], v[188:191], v[64:67]
	s_setprio 0
	s_mov_b32 m0, s57
	v_lshl_add_u64 v[214:215], s[26:27], 0, v[128:129]
	s_barrier
	ds_read_b128 v[160:163], v143 offset:16384
	ds_read_b128 v[164:167], v143 offset:17408
	ds_read_b128 v[168:171], v143 offset:18432
	ds_read_b128 v[172:175], v143 offset:19456
	ds_read_b128 v[176:179], v143 offset:20480
	ds_read_b128 v[180:183], v143 offset:21504
	ds_read_b128 v[184:187], v143 offset:22528
	ds_read_b128 v[188:191], v143 offset:23552
	global_load_lds_dwordx4 v[214:215], off
	v_lshl_add_u64 v[220:221], s[26:27], 0, v[130:131]
	s_mov_b32 m0, s60
	s_nop 0
	global_load_lds_dwordx4 v[220:221], off
	s_barrier
	s_waitcnt lgkmcnt(0)
	s_setprio 1
	s_waitcnt lgkmcnt(0)
	v_mfma_f32_16x16x32_bf16 v[60:63], v[144:147], v[160:163], v[60:63]
	v_mfma_f32_16x16x32_bf16 v[56:59], v[152:155], v[160:163], v[56:59]
	v_mfma_f32_16x16x32_bf16 v[44:47], v[144:147], v[168:171], v[44:47]
	v_mfma_f32_16x16x32_bf16 v[40:43], v[152:155], v[168:171], v[40:43]
	v_mfma_f32_16x16x32_bf16 v[28:31], v[144:147], v[176:179], v[28:31]
	v_mfma_f32_16x16x32_bf16 v[24:27], v[152:155], v[176:179], v[24:27]
	v_mfma_f32_16x16x32_bf16 v[12:15], v[144:147], v[184:187], v[12:15]
	v_mfma_f32_16x16x32_bf16 v[8:11], v[152:155], v[184:187], v[8:11]
	v_mfma_f32_16x16x32_bf16 v[60:63], v[148:151], v[164:167], v[60:63]
	v_mfma_f32_16x16x32_bf16 v[56:59], v[156:159], v[164:167], v[56:59]
	v_mfma_f32_16x16x32_bf16 v[44:47], v[148:151], v[172:175], v[44:47]
	v_mfma_f32_16x16x32_bf16 v[40:43], v[156:159], v[172:175], v[40:43]
	v_mfma_f32_16x16x32_bf16 v[28:31], v[148:151], v[180:183], v[28:31]
	v_mfma_f32_16x16x32_bf16 v[24:27], v[156:159], v[180:183], v[24:27]
	v_mfma_f32_16x16x32_bf16 v[12:15], v[148:151], v[188:191], v[12:15]
	v_mfma_f32_16x16x32_bf16 v[8:11], v[156:159], v[188:191], v[8:11]
	s_setprio 0
	s_barrier
	s_add_u32 s72, s24, 0x80000
	s_addc_u32 s73, s25, 0
	s_add_i32 s28, s65, s56
	v_lshl_add_u64 v[144:145], s[72:73], 0, v[128:129]
	s_mov_b32 m0, s28
	s_nop 0
	global_load_lds_dwordx4 v[144:145], off
	v_lshl_add_u64 v[144:145], s[72:73], 0, v[130:131]
	s_add_i32 m0, s28, 0x2000
	s_nop 0
	global_load_lds_dwordx4 v[144:145], off
	s_waitcnt vmcnt(6)
	s_barrier
	s_setprio 1
	v_mfma_f32_16x16x32_bf16 v[52:55], v[192:195], v[160:163], v[52:55]
	v_mfma_f32_16x16x32_bf16 v[48:51], v[200:203], v[160:163], v[48:51]
	v_mfma_f32_16x16x32_bf16 v[36:39], v[192:195], v[168:171], v[36:39]
	v_mfma_f32_16x16x32_bf16 v[32:35], v[200:203], v[168:171], v[32:35]
	v_mfma_f32_16x16x32_bf16 v[20:23], v[192:195], v[176:179], v[20:23]
	v_mfma_f32_16x16x32_bf16 v[16:19], v[200:203], v[176:179], v[16:19]
	v_mfma_f32_16x16x32_bf16 v[4:7], v[192:195], v[184:187], v[4:7]
	v_mfma_f32_16x16x32_bf16 v[0:3], v[200:203], v[184:187], v[0:3]
	v_mfma_f32_16x16x32_bf16 v[52:55], v[196:199], v[164:167], v[52:55]
	v_mfma_f32_16x16x32_bf16 v[48:51], v[204:207], v[164:167], v[48:51]
	v_mfma_f32_16x16x32_bf16 v[36:39], v[196:199], v[172:175], v[36:39]
	v_mfma_f32_16x16x32_bf16 v[32:35], v[204:207], v[172:175], v[32:35]
	v_mfma_f32_16x16x32_bf16 v[20:23], v[196:199], v[180:183], v[20:23]
	v_mfma_f32_16x16x32_bf16 v[16:19], v[204:207], v[180:183], v[16:19]
	v_mfma_f32_16x16x32_bf16 v[4:7], v[196:199], v[188:191], v[4:7]
	v_mfma_f32_16x16x32_bf16 v[0:3], v[204:207], v[188:191], v[0:3]
	s_setprio 0
	s_add_i32 s28, 0, 0x18000
	v_add_u32_e32 v156, s28, v139
	s_barrier
	ds_read_b128 v[144:147], v156
	ds_read_b128 v[148:151], v156 offset:1024
	ds_read_b128 v[152:155], v156 offset:2048
	ds_read_b128 v[156:159], v156 offset:3072
	s_add_u32 s26, s26, 0x80000
	s_addc_u32 s27, s27, 0
	s_mov_b32 m0, s61
	v_lshl_add_u64 v[192:193], s[26:27], 0, v[128:129]
	ds_read_b128 v[160:163], v143 offset:32768
	ds_read_b128 v[164:167], v143 offset:33792
	ds_read_b128 v[168:171], v143 offset:34816
	ds_read_b128 v[172:175], v143 offset:35840
	ds_read_b128 v[176:179], v143 offset:36864
	ds_read_b128 v[180:183], v143 offset:37888
	ds_read_b128 v[184:187], v143 offset:38912
	ds_read_b128 v[188:191], v143 offset:39936
	global_load_lds_dwordx4 v[192:193], off
	v_lshl_add_u64 v[192:193], s[26:27], 0, v[130:131]
	s_mov_b32 m0, s62
	s_nop 0
	global_load_lds_dwordx4 v[192:193], off
	s_waitcnt lgkmcnt(8)
	s_barrier
	s_waitcnt lgkmcnt(0)
	s_setprio 1
	s_waitcnt lgkmcnt(0)
	v_mfma_f32_16x16x32_bf16 v[124:127], v[144:147], v[160:163], v[124:127]
	v_mfma_f32_16x16x32_bf16 v[120:123], v[152:155], v[160:163], v[120:123]
	v_mfma_f32_16x16x32_bf16 v[108:111], v[144:147], v[168:171], v[108:111]
	v_mfma_f32_16x16x32_bf16 v[104:107], v[152:155], v[168:171], v[104:107]
	v_mfma_f32_16x16x32_bf16 v[92:95], v[144:147], v[176:179], v[92:95]
	v_mfma_f32_16x16x32_bf16 v[88:91], v[152:155], v[176:179], v[88:91]
	v_mfma_f32_16x16x32_bf16 v[76:79], v[144:147], v[184:187], v[76:79]
	v_mfma_f32_16x16x32_bf16 v[72:75], v[152:155], v[184:187], v[72:75]
	v_mfma_f32_16x16x32_bf16 v[124:127], v[148:151], v[164:167], v[124:127]
	v_mfma_f32_16x16x32_bf16 v[120:123], v[156:159], v[164:167], v[120:123]
	v_mfma_f32_16x16x32_bf16 v[108:111], v[148:151], v[172:175], v[108:111]
	v_mfma_f32_16x16x32_bf16 v[104:107], v[156:159], v[172:175], v[104:107]
	v_mfma_f32_16x16x32_bf16 v[92:95], v[148:151], v[180:183], v[92:95]
	v_mfma_f32_16x16x32_bf16 v[88:91], v[156:159], v[180:183], v[88:91]
	v_mfma_f32_16x16x32_bf16 v[76:79], v[148:151], v[188:191], v[76:79]
	v_mfma_f32_16x16x32_bf16 v[72:75], v[156:159], v[188:191], v[72:75]
	s_setprio 0
	s_barrier
	s_add_i32 s26, 0, 0x1c000
	s_add_i32 s27, s28, s56
	v_add_u32_e32 v204, s26, v139
	v_lshl_add_u64 v[136:137], v[136:137], 0, s[68:69]
	s_mov_b32 m0, s27
	ds_read_b128 v[192:195], v204
	ds_read_b128 v[196:199], v204 offset:1024
	ds_read_b128 v[200:203], v204 offset:2048
	ds_read_b128 v[204:207], v204 offset:3072
	global_load_lds_dwordx4 v[136:137], off
	v_lshl_add_u64 v[136:137], v[212:213], 0, s[68:69]
	s_add_i32 m0, s27, 0x2000
	s_nop 0
	global_load_lds_dwordx4 v[136:137], off
	s_barrier
	s_waitcnt lgkmcnt(0)
	s_setprio 1
	s_waitcnt lgkmcnt(0)
	v_mfma_f32_16x16x32_bf16 v[116:119], v[192:195], v[160:163], v[116:119]
	v_mfma_f32_16x16x32_bf16 v[112:115], v[200:203], v[160:163], v[112:115]
	v_mfma_f32_16x16x32_bf16 v[100:103], v[192:195], v[168:171], v[100:103]
	v_mfma_f32_16x16x32_bf16 v[96:99], v[200:203], v[168:171], v[96:99]
	v_mfma_f32_16x16x32_bf16 v[84:87], v[192:195], v[176:179], v[84:87]
	v_mfma_f32_16x16x32_bf16 v[80:83], v[200:203], v[176:179], v[80:83]
	v_mfma_f32_16x16x32_bf16 v[68:71], v[192:195], v[184:187], v[68:71]
	v_mfma_f32_16x16x32_bf16 v[64:67], v[200:203], v[184:187], v[64:67]
	v_mfma_f32_16x16x32_bf16 v[116:119], v[196:199], v[164:167], v[116:119]
	v_mfma_f32_16x16x32_bf16 v[112:115], v[204:207], v[164:167], v[112:115]
	v_mfma_f32_16x16x32_bf16 v[100:103], v[196:199], v[172:175], v[100:103]
	v_mfma_f32_16x16x32_bf16 v[96:99], v[204:207], v[172:175], v[96:99]
	v_mfma_f32_16x16x32_bf16 v[84:87], v[196:199], v[180:183], v[84:87]
	v_mfma_f32_16x16x32_bf16 v[80:83], v[204:207], v[180:183], v[80:83]
	v_mfma_f32_16x16x32_bf16 v[68:71], v[196:199], v[188:191], v[68:71]
	v_mfma_f32_16x16x32_bf16 v[64:67], v[204:207], v[188:191], v[64:67]
	s_setprio 0
	s_mov_b32 m0, s75
	v_lshl_add_u64 v[136:137], v[214:215], 0, s[68:69]
	s_barrier
	ds_read_b128 v[160:163], v143 offset:49152
	ds_read_b128 v[164:167], v143 offset:50176
	ds_read_b128 v[168:171], v143 offset:51200
	ds_read_b128 v[172:175], v143 offset:52224
	ds_read_b128 v[176:179], v143 offset:53248
	ds_read_b128 v[180:183], v143 offset:54272
	ds_read_b128 v[184:187], v143 offset:55296
	ds_read_b128 v[188:191], v143 offset:56320
	global_load_lds_dwordx4 v[136:137], off
	v_lshl_add_u64 v[136:137], v[220:221], 0, s[68:69]
	s_mov_b32 m0, s78
	s_nop 0
	global_load_lds_dwordx4 v[136:137], off
	s_barrier
	s_waitcnt lgkmcnt(0)
	s_setprio 1
	s_waitcnt lgkmcnt(0)
	v_mfma_f32_16x16x32_bf16 v[60:63], v[144:147], v[160:163], v[60:63]
	v_mfma_f32_16x16x32_bf16 v[56:59], v[152:155], v[160:163], v[56:59]
	v_mfma_f32_16x16x32_bf16 v[44:47], v[144:147], v[168:171], v[44:47]
	v_mfma_f32_16x16x32_bf16 v[40:43], v[152:155], v[168:171], v[40:43]
	v_mfma_f32_16x16x32_bf16 v[28:31], v[144:147], v[176:179], v[28:31]
	v_mfma_f32_16x16x32_bf16 v[24:27], v[152:155], v[176:179], v[24:27]
	v_mfma_f32_16x16x32_bf16 v[12:15], v[144:147], v[184:187], v[12:15]
	v_mfma_f32_16x16x32_bf16 v[8:11], v[152:155], v[184:187], v[8:11]
	v_mfma_f32_16x16x32_bf16 v[60:63], v[148:151], v[164:167], v[60:63]
	v_mfma_f32_16x16x32_bf16 v[56:59], v[156:159], v[164:167], v[56:59]
	v_mfma_f32_16x16x32_bf16 v[44:47], v[148:151], v[172:175], v[44:47]
	v_mfma_f32_16x16x32_bf16 v[40:43], v[156:159], v[172:175], v[40:43]
	v_mfma_f32_16x16x32_bf16 v[28:31], v[148:151], v[180:183], v[28:31]
	v_mfma_f32_16x16x32_bf16 v[24:27], v[156:159], v[180:183], v[24:27]
	v_mfma_f32_16x16x32_bf16 v[12:15], v[148:151], v[188:191], v[12:15]
	v_mfma_f32_16x16x32_bf16 v[8:11], v[156:159], v[188:191], v[8:11]
	s_setprio 0
	s_barrier
	s_add_u32 s24, s24, 0x80080
	s_addc_u32 s25, s25, 0
	s_add_i32 s26, s26, s56
	v_lshl_add_u64 v[136:137], s[24:25], 0, v[128:129]
	s_mov_b32 m0, s26
	s_nop 0
	global_load_lds_dwordx4 v[136:137], off
	v_lshl_add_u64 v[136:137], s[24:25], 0, v[130:131]
	s_add_i32 m0, s26, 0x2000
	s_nop 0
	global_load_lds_dwordx4 v[136:137], off
	s_waitcnt vmcnt(6)
	s_barrier
	s_setprio 1
	v_mfma_f32_16x16x32_bf16 v[52:55], v[192:195], v[160:163], v[52:55]
	v_mfma_f32_16x16x32_bf16 v[48:51], v[200:203], v[160:163], v[48:51]
	v_mfma_f32_16x16x32_bf16 v[36:39], v[192:195], v[168:171], v[36:39]
	v_mfma_f32_16x16x32_bf16 v[32:35], v[200:203], v[168:171], v[32:35]
	v_mfma_f32_16x16x32_bf16 v[20:23], v[192:195], v[176:179], v[20:23]
	v_mfma_f32_16x16x32_bf16 v[16:19], v[200:203], v[176:179], v[16:19]
	v_mfma_f32_16x16x32_bf16 v[4:7], v[192:195], v[184:187], v[4:7]
	v_mfma_f32_16x16x32_bf16 v[0:3], v[200:203], v[184:187], v[0:3]
	v_mfma_f32_16x16x32_bf16 v[52:55], v[196:199], v[164:167], v[52:55]
	v_mfma_f32_16x16x32_bf16 v[48:51], v[204:207], v[164:167], v[48:51]
	v_mfma_f32_16x16x32_bf16 v[36:39], v[196:199], v[172:175], v[36:39]
	v_mfma_f32_16x16x32_bf16 v[32:35], v[204:207], v[172:175], v[32:35]
	v_mfma_f32_16x16x32_bf16 v[20:23], v[196:199], v[180:183], v[20:23]
	v_mfma_f32_16x16x32_bf16 v[16:19], v[204:207], v[180:183], v[16:19]
	v_mfma_f32_16x16x32_bf16 v[4:7], v[196:199], v[188:191], v[4:7]
	v_mfma_f32_16x16x32_bf16 v[0:3], v[204:207], v[188:191], v[0:3]
	s_setprio 0
	s_add_i32 s64, s64, 2
	s_add_u32 s22, s22, 0x100
	s_addc_u32 s23, s23, 0
	s_add_u32 s2, s2, 0x100
	s_addc_u32 s3, s3, 0
	s_cmp_gt_u32 s64, 13
	s_barrier
	s_cbranch_scc0 .LBB0_272
	s_ashr_i32 s19, s18, 31
	s_lshl_b64 s[2:3], s[18:19], 24
	s_add_u32 s18, s63, s2
	s_addc_u32 s19, s74, s3
	s_lshl_b32 s2, s20, 8
	v_add_u32_e32 v136, s2, v138
	v_ashrrev_i32_e32 v137, 31, v136
	v_lshl_add_u64 v[146:147], v[136:137], 2, s[4:5]
	global_load_dword v222, v[146:147], off
	global_load_dword v223, v[146:147], off offset:64
	global_load_dword v224, v[146:147], off offset:128
	global_load_dword v225, v[146:147], off offset:192
	global_load_dword v226, v[146:147], off offset:512
	global_load_dword v227, v[146:147], off offset:576
	global_load_dword v228, v[146:147], off offset:640
	global_load_dword v229, v[146:147], off offset:704
	s_lshl_b32 s20, s21, 8
	v_lshlrev_b64 v[144:145], 11, v[136:137]
	s_ashr_i32 s21, s20, 31
	v_lshl_add_u64 v[144:145], s[18:19], 0, v[144:145]
	s_lshl_b64 s[20:21], s[20:21], 1
	v_lshl_add_u64 v[144:145], v[144:145], 0, s[20:21]
	v_lshl_add_u64 v[144:145], v[144:145], 0, s[50:51]
	v_lshl_add_u64 v[144:145], v[144:145], 0, v[208:209]
	s_and_b64 vcc, exec, s[16:17]
	s_mov_b64 s[24:25], s[14:15]
	s_mov_b64 s[22:23], s[12:13]
	s_mov_b32 s85, 0xfe5163ab
	s_waitcnt vmcnt(0)
	v_mov_b32_e32 v146, v222
	v_pk_mul_f32 v[126:127], v[126:127], v[146:147] op_sel_hi:[1,0]
	v_pk_mul_f32 v[124:125], v[124:125], v[146:147] op_sel_hi:[1,0]
	v_pk_mul_f32 v[148:149], v[122:123], v[146:147] op_sel_hi:[1,0]
	v_pk_mul_f32 v[122:123], v[120:121], v[146:147] op_sel_hi:[1,0]
	v_cvt_pk_bf16_f32 v120, v124, v125
	v_cvt_pk_bf16_f32 v121, v126, v127
	v_cvt_pk_bf16_f32 v122, v122, v123
	v_cvt_pk_bf16_f32 v123, v148, v149
	global_store_dwordx4 v[144:145], v[120:123], off
	v_pk_mul_f32 v[118:119], v[118:119], v[146:147] op_sel_hi:[1,0]
	v_pk_mul_f32 v[116:117], v[116:117], v[146:147] op_sel_hi:[1,0]
	v_pk_mul_f32 v[120:121], v[114:115], v[146:147] op_sel_hi:[1,0]
	v_pk_mul_f32 v[114:115], v[112:113], v[146:147] op_sel_hi:[1,0]
	v_cvt_pk_bf16_f32 v112, v116, v117
	v_cvt_pk_bf16_f32 v113, v118, v119
	v_cvt_pk_bf16_f32 v114, v114, v115
	v_cvt_pk_bf16_f32 v115, v120, v121
	global_store_dwordx4 v[144:145], v[112:115], off offset:256
	s_nop 1
	v_add_u32_e32 v112, s2, v140
	v_ashrrev_i32_e32 v113, 31, v112
	v_lshlrev_b64 v[114:115], 11, v[112:113]
	v_lshl_add_u64 v[112:113], v[112:113], 2, s[4:5]
	v_lshl_add_u64 v[114:115], s[18:19], 0, v[114:115]
	v_lshl_add_u64 v[114:115], v[114:115], 0, s[20:21]
	v_lshl_add_u64 v[114:115], v[114:115], 0, s[50:51]
	v_lshl_add_u64 v[114:115], v[114:115], 0, v[208:209]
	v_mov_b32_e32 v112, v223
	v_pk_mul_f32 v[110:111], v[110:111], v[112:113] op_sel_hi:[1,0]
	v_pk_mul_f32 v[108:109], v[108:109], v[112:113] op_sel_hi:[1,0]
	v_pk_mul_f32 v[116:117], v[106:107], v[112:113] op_sel_hi:[1,0]
	v_pk_mul_f32 v[106:107], v[104:105], v[112:113] op_sel_hi:[1,0]
	v_cvt_pk_bf16_f32 v104, v108, v109
	v_cvt_pk_bf16_f32 v105, v110, v111
	v_cvt_pk_bf16_f32 v106, v106, v107
	v_cvt_pk_bf16_f32 v107, v116, v117
	global_store_dwordx4 v[114:115], v[104:107], off
	v_pk_mul_f32 v[102:103], v[102:103], v[112:113] op_sel_hi:[1,0]
	v_pk_mul_f32 v[100:101], v[100:101], v[112:113] op_sel_hi:[1,0]
	v_pk_mul_f32 v[104:105], v[98:99], v[112:113] op_sel_hi:[1,0]
	v_pk_mul_f32 v[98:99], v[96:97], v[112:113] op_sel_hi:[1,0]
	v_cvt_pk_bf16_f32 v96, v100, v101
	v_cvt_pk_bf16_f32 v97, v102, v103
	v_cvt_pk_bf16_f32 v98, v98, v99
	v_cvt_pk_bf16_f32 v99, v104, v105
	global_store_dwordx4 v[114:115], v[96:99], off offset:256
	s_nop 1
	v_add_u32_e32 v96, s2, v141
	v_ashrrev_i32_e32 v97, 31, v96
	v_lshlrev_b64 v[98:99], 11, v[96:97]
	v_lshl_add_u64 v[96:97], v[96:97], 2, s[4:5]
	v_lshl_add_u64 v[98:99], s[18:19], 0, v[98:99]
	v_lshl_add_u64 v[98:99], v[98:99], 0, s[20:21]
	v_lshl_add_u64 v[98:99], v[98:99], 0, s[50:51]
	v_lshl_add_u64 v[98:99], v[98:99], 0, v[208:209]
	v_mov_b32_e32 v96, v224
	v_pk_mul_f32 v[94:95], v[94:95], v[96:97] op_sel_hi:[1,0]
	v_pk_mul_f32 v[92:93], v[92:93], v[96:97] op_sel_hi:[1,0]
	v_pk_mul_f32 v[100:101], v[90:91], v[96:97] op_sel_hi:[1,0]
	v_pk_mul_f32 v[90:91], v[88:89], v[96:97] op_sel_hi:[1,0]
	v_cvt_pk_bf16_f32 v88, v92, v93
	v_cvt_pk_bf16_f32 v89, v94, v95
	v_cvt_pk_bf16_f32 v90, v90, v91
	v_cvt_pk_bf16_f32 v91, v100, v101
	global_store_dwordx4 v[98:99], v[88:91], off
	v_pk_mul_f32 v[86:87], v[86:87], v[96:97] op_sel_hi:[1,0]
	v_pk_mul_f32 v[84:85], v[84:85], v[96:97] op_sel_hi:[1,0]
	v_pk_mul_f32 v[88:89], v[82:83], v[96:97] op_sel_hi:[1,0]
	v_pk_mul_f32 v[82:83], v[80:81], v[96:97] op_sel_hi:[1,0]
	v_cvt_pk_bf16_f32 v80, v84, v85
	v_cvt_pk_bf16_f32 v81, v86, v87
	v_cvt_pk_bf16_f32 v82, v82, v83
	v_cvt_pk_bf16_f32 v83, v88, v89
	global_store_dwordx4 v[98:99], v[80:83], off offset:256
	s_nop 1
	v_add_u32_e32 v80, s2, v142
	v_ashrrev_i32_e32 v81, 31, v80
	v_lshlrev_b64 v[82:83], 11, v[80:81]
	v_lshl_add_u64 v[80:81], v[80:81], 2, s[4:5]
	v_lshl_add_u64 v[82:83], s[18:19], 0, v[82:83]
	v_lshl_add_u64 v[82:83], v[82:83], 0, s[20:21]
	v_lshl_add_u64 v[82:83], v[82:83], 0, s[50:51]
	v_lshl_add_u64 v[82:83], v[82:83], 0, v[208:209]
	v_mov_b32_e32 v80, v225
	v_pk_mul_f32 v[78:79], v[78:79], v[80:81] op_sel_hi:[1,0]
	v_pk_mul_f32 v[76:77], v[76:77], v[80:81] op_sel_hi:[1,0]
	v_pk_mul_f32 v[84:85], v[74:75], v[80:81] op_sel_hi:[1,0]
	v_pk_mul_f32 v[74:75], v[72:73], v[80:81] op_sel_hi:[1,0]
	v_cvt_pk_bf16_f32 v72, v76, v77
	v_cvt_pk_bf16_f32 v73, v78, v79
	v_cvt_pk_bf16_f32 v74, v74, v75
	v_cvt_pk_bf16_f32 v75, v84, v85
	global_store_dwordx4 v[82:83], v[72:75], off
	v_pk_mul_f32 v[70:71], v[70:71], v[80:81] op_sel_hi:[1,0]
	v_pk_mul_f32 v[68:69], v[68:69], v[80:81] op_sel_hi:[1,0]
	v_pk_mul_f32 v[72:73], v[66:67], v[80:81] op_sel_hi:[1,0]
	v_pk_mul_f32 v[66:67], v[64:65], v[80:81] op_sel_hi:[1,0]
	v_cvt_pk_bf16_f32 v64, v68, v69
	v_cvt_pk_bf16_f32 v65, v70, v71
	v_cvt_pk_bf16_f32 v66, v66, v67
	v_cvt_pk_bf16_f32 v67, v72, v73
	global_store_dwordx4 v[82:83], v[64:67], off offset:256
	s_nop 1
	v_add_u32_e32 v64, 0x80, v136
	v_ashrrev_i32_e32 v65, 31, v64
	v_lshlrev_b64 v[66:67], 11, v[64:65]
	v_lshl_add_u64 v[64:65], v[64:65], 2, s[4:5]
	v_lshl_add_u64 v[66:67], s[18:19], 0, v[66:67]
	v_lshl_add_u64 v[66:67], v[66:67], 0, s[20:21]
	v_lshl_add_u64 v[66:67], v[66:67], 0, s[50:51]
	v_lshl_add_u64 v[66:67], v[66:67], 0, v[208:209]
	v_mov_b32_e32 v64, v226
	v_pk_mul_f32 v[62:63], v[62:63], v[64:65] op_sel_hi:[1,0]
	v_pk_mul_f32 v[60:61], v[60:61], v[64:65] op_sel_hi:[1,0]
	v_pk_mul_f32 v[68:69], v[58:59], v[64:65] op_sel_hi:[1,0]
	v_pk_mul_f32 v[58:59], v[56:57], v[64:65] op_sel_hi:[1,0]
	v_cvt_pk_bf16_f32 v56, v60, v61
	v_cvt_pk_bf16_f32 v57, v62, v63
	v_cvt_pk_bf16_f32 v58, v58, v59
	v_cvt_pk_bf16_f32 v59, v68, v69
	global_store_dwordx4 v[66:67], v[56:59], off
	v_pk_mul_f32 v[54:55], v[54:55], v[64:65] op_sel_hi:[1,0]
	v_pk_mul_f32 v[52:53], v[52:53], v[64:65] op_sel_hi:[1,0]
	v_pk_mul_f32 v[56:57], v[50:51], v[64:65] op_sel_hi:[1,0]
	v_pk_mul_f32 v[50:51], v[48:49], v[64:65] op_sel_hi:[1,0]
	v_cvt_pk_bf16_f32 v48, v52, v53
	v_cvt_pk_bf16_f32 v49, v54, v55
	v_cvt_pk_bf16_f32 v50, v50, v51
	v_cvt_pk_bf16_f32 v51, v56, v57
	global_store_dwordx4 v[66:67], v[48:51], off offset:256
	s_nop 1
	v_add_u32_e32 v48, 0x90, v136
	v_ashrrev_i32_e32 v49, 31, v48
	v_lshlrev_b64 v[50:51], 11, v[48:49]
	v_lshl_add_u64 v[48:49], v[48:49], 2, s[4:5]
	v_lshl_add_u64 v[50:51], s[18:19], 0, v[50:51]
	v_lshl_add_u64 v[50:51], v[50:51], 0, s[20:21]
	v_lshl_add_u64 v[50:51], v[50:51], 0, s[50:51]
	v_lshl_add_u64 v[50:51], v[50:51], 0, v[208:209]
	v_mov_b32_e32 v48, v227
	v_pk_mul_f32 v[46:47], v[46:47], v[48:49] op_sel_hi:[1,0]
	v_pk_mul_f32 v[44:45], v[44:45], v[48:49] op_sel_hi:[1,0]
	v_pk_mul_f32 v[52:53], v[42:43], v[48:49] op_sel_hi:[1,0]
	v_pk_mul_f32 v[42:43], v[40:41], v[48:49] op_sel_hi:[1,0]
	v_cvt_pk_bf16_f32 v40, v44, v45
	v_cvt_pk_bf16_f32 v41, v46, v47
	v_cvt_pk_bf16_f32 v42, v42, v43
	v_cvt_pk_bf16_f32 v43, v52, v53
	global_store_dwordx4 v[50:51], v[40:43], off
	v_pk_mul_f32 v[38:39], v[38:39], v[48:49] op_sel_hi:[1,0]
	v_pk_mul_f32 v[36:37], v[36:37], v[48:49] op_sel_hi:[1,0]
	v_pk_mul_f32 v[40:41], v[34:35], v[48:49] op_sel_hi:[1,0]
	v_pk_mul_f32 v[34:35], v[32:33], v[48:49] op_sel_hi:[1,0]
	v_cvt_pk_bf16_f32 v32, v36, v37
	v_cvt_pk_bf16_f32 v33, v38, v39
	v_cvt_pk_bf16_f32 v34, v34, v35
	v_cvt_pk_bf16_f32 v35, v40, v41
	global_store_dwordx4 v[50:51], v[32:35], off offset:256
	s_nop 1
	v_add_u32_e32 v32, 0xa0, v136
	v_ashrrev_i32_e32 v33, 31, v32
	v_lshlrev_b64 v[34:35], 11, v[32:33]
	v_lshl_add_u64 v[32:33], v[32:33], 2, s[4:5]
	v_lshl_add_u64 v[34:35], s[18:19], 0, v[34:35]
	v_lshl_add_u64 v[34:35], v[34:35], 0, s[20:21]
	v_lshl_add_u64 v[34:35], v[34:35], 0, s[50:51]
	v_lshl_add_u64 v[34:35], v[34:35], 0, v[208:209]
	v_mov_b32_e32 v32, v228
	v_pk_mul_f32 v[30:31], v[30:31], v[32:33] op_sel_hi:[1,0]
	v_pk_mul_f32 v[28:29], v[28:29], v[32:33] op_sel_hi:[1,0]
	v_pk_mul_f32 v[36:37], v[26:27], v[32:33] op_sel_hi:[1,0]
	v_pk_mul_f32 v[26:27], v[24:25], v[32:33] op_sel_hi:[1,0]
	v_cvt_pk_bf16_f32 v24, v28, v29
	v_cvt_pk_bf16_f32 v25, v30, v31
	v_cvt_pk_bf16_f32 v26, v26, v27
	v_cvt_pk_bf16_f32 v27, v36, v37
	global_store_dwordx4 v[34:35], v[24:27], off
	v_pk_mul_f32 v[22:23], v[22:23], v[32:33] op_sel_hi:[1,0]
	v_pk_mul_f32 v[20:21], v[20:21], v[32:33] op_sel_hi:[1,0]
	v_pk_mul_f32 v[24:25], v[18:19], v[32:33] op_sel_hi:[1,0]
	v_pk_mul_f32 v[18:19], v[16:17], v[32:33] op_sel_hi:[1,0]
	v_cvt_pk_bf16_f32 v16, v20, v21
	v_cvt_pk_bf16_f32 v17, v22, v23
	v_cvt_pk_bf16_f32 v18, v18, v19
	v_cvt_pk_bf16_f32 v19, v24, v25
	global_store_dwordx4 v[34:35], v[16:19], off offset:256
	s_nop 1
	v_add_u32_e32 v16, 0xb0, v136
	v_ashrrev_i32_e32 v17, 31, v16
	v_lshl_add_u64 v[18:19], v[16:17], 2, s[4:5]
	v_lshlrev_b64 v[16:17], 11, v[16:17]
	v_lshl_add_u64 v[16:17], s[18:19], 0, v[16:17]
	v_lshl_add_u64 v[16:17], v[16:17], 0, s[20:21]
	v_lshl_add_u64 v[16:17], v[16:17], 0, s[50:51]
	v_lshl_add_u64 v[16:17], v[16:17], 0, v[208:209]
	s_mov_b32 s21, s91
	s_mov_b32 s20, s6
	s_mov_b32 s18, s7
	v_mov_b32_e32 v18, v229
	v_pk_mul_f32 v[14:15], v[14:15], v[18:19] op_sel_hi:[1,0]
	v_pk_mul_f32 v[12:13], v[12:13], v[18:19] op_sel_hi:[1,0]
	v_pk_mul_f32 v[20:21], v[10:11], v[18:19] op_sel_hi:[1,0]
	v_pk_mul_f32 v[10:11], v[8:9], v[18:19] op_sel_hi:[1,0]
	v_cvt_pk_bf16_f32 v8, v12, v13
	v_cvt_pk_bf16_f32 v9, v14, v15
	v_cvt_pk_bf16_f32 v10, v10, v11
	v_cvt_pk_bf16_f32 v11, v20, v21
	global_store_dwordx4 v[16:17], v[8:11], off
	v_pk_mul_f32 v[6:7], v[6:7], v[18:19] op_sel_hi:[1,0]
	v_pk_mul_f32 v[4:5], v[4:5], v[18:19] op_sel_hi:[1,0]
	v_pk_mul_f32 v[8:9], v[2:3], v[18:19] op_sel_hi:[1,0]
	v_pk_mul_f32 v[2:3], v[0:1], v[18:19] op_sel_hi:[1,0]
	v_cvt_pk_bf16_f32 v0, v4, v5
	v_cvt_pk_bf16_f32 v1, v6, v7
	v_cvt_pk_bf16_f32 v2, v2, v3
	v_cvt_pk_bf16_f32 v3, v8, v9
	global_store_dwordx4 v[16:17], v[0:3], off offset:256
	s_cbranch_vccz .LBB0_264
	s_waitcnt vmcnt(0)
	s_cmpk_gt_u32 s40, 0xff
	s_cbranch_scc1 .LBB0_276
	s_barrier

.LBB0_454:
	s_sext_i32_i8 s21, s8
	v_readlane_b32 s8, v255, 21
	v_bfe_u32 v16, v14, 4, 2
	s_add_u32 s4, s4, s8
	v_and_b32_e32 v15, 15, v14
	v_lshlrev_b32_e32 v17, 4, v16
	v_lshlrev_b32_e32 v14, 2, v14
	s_addc_u32 s5, s5, 0
	s_and_b32 s8, s2, 3
	v_lshl_or_b32 v160, s3, 6, v15
	v_lshl_or_b32 v15, v15, 6, v17
	s_lshl_b32 s2, s3, 13
	v_and_b32_e32 v14, 32, v14
	s_add_i32 m0, s56, 0x18000
	v_lshl_add_u64 v[6:7], v[6:7], 0, s[68:69]
	v_bitop3_b32 v17, v15, s2, v14 bitop3:0xde
	s_lshl_b32 s2, s8, 12
	s_waitcnt vmcnt(4)
	s_barrier
	global_load_lds_dwordx4 v[6:7], off
	v_lshl_add_u64 v[4:5], v[4:5], 0, s[68:69]
	s_add_i32 m0, s56, 0x1a000
	s_add_i32 s62, s56, 0x8000
	s_add_i32 s63, s56, 0xa000
	v_bitop3_b32 v161, s2, v15, v14 bitop3:0xf6
	global_load_lds_dwordx4 v[4:5], off
	v_lshl_add_u64 v[2:3], v[2:3], 0, s[68:69]
	s_mov_b32 m0, s62
	s_add_u32 s2, s24, 0x40080
	global_load_lds_dwordx4 v[2:3], off
	v_lshl_add_u64 v[0:1], v[0:1], 0, s[68:69]
	s_mov_b32 m0, s63
	s_addc_u32 s3, s25, 0
	global_load_lds_dwordx4 v[0:1], off
	s_add_i32 m0, s56, 0x1c000
	v_lshl_add_u64 v[0:1], s[2:3], 0, v[208:209]
	global_load_lds_dwordx4 v[0:1], off
	v_lshl_add_u64 v[0:1], s[2:3], 0, v[128:129]
	s_add_i32 m0, s56, 0x1e000
	s_lshl_b32 s74, s8, 4
	global_load_lds_dwordx4 v[0:1], off
	v_lshlrev_b32_e32 v0, 3, v16
	v_mov_b32_e32 v1, v209
	v_lshl_add_u64 v[130:131], s[4:5], 0, v[0:1]
	v_lshlrev_b32_e32 v0, 14, v8
	v_and_b32_e32 v0, 0xffff8000, v0
	v_lshl_add_u32 v0, v9, 11, v0
	v_and_b32_e32 v1, 1, v8
	v_lshl_or_b32 v0, v1, 6, v0
	v_lshl_add_u32 v132, v10, 1, v0
	v_lshlrev_b32_e32 v0, 14, v11
	v_and_b32_e32 v0, 0xffff8000, v0
	s_waitcnt vmcnt(6)
	v_lshl_add_u32 v0, v12, 11, v0
	v_and_b32_e32 v1, 1, v11
	v_lshl_or_b32 v0, v1, 6, v0
	s_ashr_i32 s75, s30, 31
	v_mov_b32_e32 v133, v209
	v_lshl_add_u32 v134, v13, 1, v0
	v_mov_b32_e32 v135, v209
	s_mov_b32 s78, 0
	v_add_u32_e32 v162, 0, v17
	s_barrier

.LBB0_528:
	v_cmp_lt_i64_e32 vcc, s[16:17], v[216:217]
	s_add_u32 s16, s41, s12
	s_addc_u32 s17, s42, s13
	s_and_b64 s[18:19], vcc, exec
	s_cselect_b32 s9, s17, s23
	s_cselect_b32 s11, s16, s22
	s_add_u32 s18, s43, s14
	s_addc_u32 s19, s46, s15
	s_and_b64 s[26:27], vcc, exec
	s_cselect_b32 s79, s19, s25
	s_cselect_b32 s84, s18, s24
	s_add_u32 s22, s22, 0x80080
	s_addc_u32 s23, s23, 0
	s_add_u32 s85, s24, 0x100
	v_mov_b32_e32 v0, 0
	s_addc_u32 s64, s25, 0
	s_mov_b32 s65, -2
	v_mov_b32_e32 v1, v0
	v_mov_b32_e32 v2, v0
	v_mov_b32_e32 v3, v0
	v_mov_b32_e32 v4, v0
	v_mov_b32_e32 v5, v0
	v_mov_b32_e32 v6, v0
	v_mov_b32_e32 v7, v0
	v_mov_b32_e32 v16, v0
	v_mov_b32_e32 v17, v0
	v_mov_b32_e32 v18, v0
	v_mov_b32_e32 v19, v0
	v_mov_b32_e32 v20, v0
	v_mov_b32_e32 v21, v0
	v_mov_b32_e32 v22, v0
	v_mov_b32_e32 v23, v0
	v_mov_b32_e32 v32, v0
	v_mov_b32_e32 v33, v0
	v_mov_b32_e32 v34, v0
	v_mov_b32_e32 v35, v0
	v_mov_b32_e32 v36, v0
	v_mov_b32_e32 v37, v0
	v_mov_b32_e32 v38, v0
	v_mov_b32_e32 v39, v0
	v_mov_b32_e32 v48, v0
	v_mov_b32_e32 v49, v0
	v_mov_b32_e32 v50, v0
	v_mov_b32_e32 v51, v0
	v_mov_b32_e32 v52, v0
	v_mov_b32_e32 v53, v0
	v_mov_b32_e32 v54, v0
	v_mov_b32_e32 v55, v0
	v_mov_b32_e32 v8, v0
	v_mov_b32_e32 v9, v0
	v_mov_b32_e32 v10, v0
	v_mov_b32_e32 v11, v0
	v_mov_b32_e32 v12, v0
	v_mov_b32_e32 v13, v0
	v_mov_b32_e32 v14, v0
	v_mov_b32_e32 v15, v0
	v_mov_b32_e32 v24, v0
	v_mov_b32_e32 v25, v0
	v_mov_b32_e32 v26, v0
	v_mov_b32_e32 v27, v0
	v_mov_b32_e32 v28, v0
	v_mov_b32_e32 v29, v0
	v_mov_b32_e32 v30, v0
	v_mov_b32_e32 v31, v0
	v_mov_b32_e32 v40, v0
	v_mov_b32_e32 v41, v0
	v_mov_b32_e32 v42, v0
	v_mov_b32_e32 v43, v0
	v_mov_b32_e32 v44, v0
	v_mov_b32_e32 v45, v0
	v_mov_b32_e32 v46, v0
	v_mov_b32_e32 v47, v0
	v_mov_b32_e32 v56, v0
	v_mov_b32_e32 v57, v0
	v_mov_b32_e32 v58, v0
	v_mov_b32_e32 v59, v0
	v_mov_b32_e32 v60, v0
	v_mov_b32_e32 v61, v0
	v_mov_b32_e32 v62, v0
	v_mov_b32_e32 v63, v0
	v_mov_b32_e32 v64, v0
	v_mov_b32_e32 v65, v0
	v_mov_b32_e32 v66, v0
	v_mov_b32_e32 v67, v0
	v_mov_b32_e32 v68, v0
	v_mov_b32_e32 v69, v0
	v_mov_b32_e32 v70, v0
	v_mov_b32_e32 v71, v0
	v_mov_b32_e32 v80, v0
	v_mov_b32_e32 v81, v0
	v_mov_b32_e32 v82, v0
	v_mov_b32_e32 v83, v0
	v_mov_b32_e32 v84, v0
	v_mov_b32_e32 v85, v0
	v_mov_b32_e32 v86, v0
	v_mov_b32_e32 v87, v0
	v_mov_b32_e32 v96, v0
	v_mov_b32_e32 v97, v0
	v_mov_b32_e32 v98, v0
	v_mov_b32_e32 v99, v0
	v_mov_b32_e32 v100, v0
	v_mov_b32_e32 v101, v0
	v_mov_b32_e32 v102, v0
	v_mov_b32_e32 v103, v0
	v_mov_b32_e32 v112, v0
	v_mov_b32_e32 v113, v0
	v_mov_b32_e32 v114, v0
	v_mov_b32_e32 v115, v0
	v_mov_b32_e32 v116, v0
	v_mov_b32_e32 v117, v0
	v_mov_b32_e32 v118, v0
	v_mov_b32_e32 v119, v0
	v_mov_b32_e32 v72, v0
	v_mov_b32_e32 v73, v0
	v_mov_b32_e32 v74, v0
	v_mov_b32_e32 v75, v0
	v_mov_b32_e32 v76, v0
	v_mov_b32_e32 v77, v0
	v_mov_b32_e32 v78, v0
	v_mov_b32_e32 v79, v0
	v_mov_b32_e32 v88, v0
	v_mov_b32_e32 v89, v0
	v_mov_b32_e32 v90, v0
	v_mov_b32_e32 v91, v0
	v_mov_b32_e32 v92, v0
	v_mov_b32_e32 v93, v0
	v_mov_b32_e32 v94, v0
	v_mov_b32_e32 v95, v0
	v_mov_b32_e32 v104, v0
	v_mov_b32_e32 v105, v0
	v_mov_b32_e32 v106, v0
	v_mov_b32_e32 v107, v0
	v_mov_b32_e32 v108, v0
	v_mov_b32_e32 v109, v0
	v_mov_b32_e32 v110, v0
	v_mov_b32_e32 v111, v0
	v_mov_b32_e32 v120, v0
	v_mov_b32_e32 v121, v0
	v_mov_b32_e32 v122, v0
	v_mov_b32_e32 v123, v0
	v_mov_b32_e32 v124, v0
	v_mov_b32_e32 v125, v0
	v_mov_b32_e32 v126, v0
	v_mov_b32_e32 v127, v0
.LBB0_529:
	s_add_u32 s24, s22, 0xfff80080
	s_addc_u32 s25, s23, -1
	s_add_i32 s28, 0, 0x10000
	v_add_u32_e32 v143, s28, v141
	ds_read_b128 v[136:139], v143
	ds_read_b128 v[144:147], v143 offset:1024
	ds_read_b128 v[148:151], v143 offset:2048
	ds_read_b128 v[152:155], v143 offset:3072
	s_cmp_eq_u32 s65, 28
	s_cselect_b32 s27, s9, s25
	s_cselect_b32 s26, s11, s24
	s_cselect_b32 s25, s79, s64
	s_cselect_b32 s24, s84, s85
	v_lshl_add_u64 v[188:189], s[22:23], 0, v[132:133]
	s_add_i32 m0, s57, 0xc000
	ds_read_b128 v[156:159], v142
	ds_read_b128 v[160:163], v142 offset:1024
	ds_read_b128 v[164:167], v142 offset:2048
	ds_read_b128 v[168:171], v142 offset:3072
	ds_read_b128 v[172:175], v142 offset:4096
	ds_read_b128 v[176:179], v142 offset:5120
	ds_read_b128 v[180:183], v142 offset:6144
	ds_read_b128 v[184:187], v142 offset:7168
	global_load_lds_dwordx4 v[188:189], off
	v_lshl_add_u64 v[188:189], s[22:23], 0, v[134:135]
	s_add_i32 m0, s57, 0xe000
	s_nop 0
	global_load_lds_dwordx4 v[188:189], off
	s_waitcnt lgkmcnt(8)
	s_barrier
	s_waitcnt lgkmcnt(0)
	s_setprio 1
	s_waitcnt lgkmcnt(0)
	v_mfma_f32_16x16x32_bf16 v[124:127], v[136:139], v[156:159], v[124:127]
	v_mfma_f32_16x16x32_bf16 v[120:123], v[148:151], v[156:159], v[120:123]
	v_mfma_f32_16x16x32_bf16 v[108:111], v[136:139], v[164:167], v[108:111]
	v_mfma_f32_16x16x32_bf16 v[104:107], v[148:151], v[164:167], v[104:107]
	v_mfma_f32_16x16x32_bf16 v[92:95], v[136:139], v[172:175], v[92:95]
	v_mfma_f32_16x16x32_bf16 v[88:91], v[148:151], v[172:175], v[88:91]
	v_mfma_f32_16x16x32_bf16 v[76:79], v[136:139], v[180:183], v[76:79]
	v_mfma_f32_16x16x32_bf16 v[72:75], v[148:151], v[180:183], v[72:75]
	v_mfma_f32_16x16x32_bf16 v[124:127], v[144:147], v[160:163], v[124:127]
	v_mfma_f32_16x16x32_bf16 v[120:123], v[152:155], v[160:163], v[120:123]
	v_mfma_f32_16x16x32_bf16 v[108:111], v[144:147], v[168:171], v[108:111]
	v_mfma_f32_16x16x32_bf16 v[104:107], v[152:155], v[168:171], v[104:107]
	v_mfma_f32_16x16x32_bf16 v[92:95], v[144:147], v[176:179], v[92:95]
	v_mfma_f32_16x16x32_bf16 v[88:91], v[152:155], v[176:179], v[88:91]
	v_mfma_f32_16x16x32_bf16 v[76:79], v[144:147], v[184:187], v[76:79]
	v_mfma_f32_16x16x32_bf16 v[72:75], v[152:155], v[184:187], v[72:75]
	s_setprio 0
	s_barrier
	s_add_i32 s72, 0, 0x14000
	s_add_i32 s28, s28, s47
	v_add_u32_e32 v143, s72, v141
	v_lshl_add_u64 v[204:205], s[24:25], 0, v[130:131]
	s_mov_b32 m0, s28
	ds_read_b128 v[188:191], v143
	ds_read_b128 v[192:195], v143 offset:1024
	ds_read_b128 v[196:199], v143 offset:2048
	ds_read_b128 v[200:203], v143 offset:3072
	global_load_lds_dwordx4 v[204:205], off
	v_lshl_add_u64 v[206:207], s[24:25], 0, v[128:129]
	s_add_i32 m0, s28, 0x2000
	s_nop 0
	global_load_lds_dwordx4 v[206:207], off
	s_barrier
	s_waitcnt lgkmcnt(0)
	s_setprio 1
	s_waitcnt lgkmcnt(0)
	v_mfma_f32_16x16x32_bf16 v[116:119], v[188:191], v[156:159], v[116:119]
	v_mfma_f32_16x16x32_bf16 v[112:115], v[196:199], v[156:159], v[112:115]
	v_mfma_f32_16x16x32_bf16 v[100:103], v[188:191], v[164:167], v[100:103]
	v_mfma_f32_16x16x32_bf16 v[96:99], v[196:199], v[164:167], v[96:99]
	v_mfma_f32_16x16x32_bf16 v[84:87], v[188:191], v[172:175], v[84:87]
	v_mfma_f32_16x16x32_bf16 v[80:83], v[196:199], v[172:175], v[80:83]
	v_mfma_f32_16x16x32_bf16 v[68:71], v[188:191], v[180:183], v[68:71]
	v_mfma_f32_16x16x32_bf16 v[64:67], v[196:199], v[180:183], v[64:67]
	v_mfma_f32_16x16x32_bf16 v[116:119], v[192:195], v[160:163], v[116:119]
	v_mfma_f32_16x16x32_bf16 v[112:115], v[200:203], v[160:163], v[112:115]
	v_mfma_f32_16x16x32_bf16 v[100:103], v[192:195], v[168:171], v[100:103]
	v_mfma_f32_16x16x32_bf16 v[96:99], v[200:203], v[168:171], v[96:99]
	v_mfma_f32_16x16x32_bf16 v[84:87], v[192:195], v[176:179], v[84:87]
	v_mfma_f32_16x16x32_bf16 v[80:83], v[200:203], v[176:179], v[80:83]
	v_mfma_f32_16x16x32_bf16 v[68:71], v[192:195], v[184:187], v[68:71]
	v_mfma_f32_16x16x32_bf16 v[64:67], v[200:203], v[184:187], v[64:67]
	s_setprio 0
	s_mov_b32 m0, s57
	v_lshl_add_u64 v[212:213], s[26:27], 0, v[130:131]
	s_barrier
	ds_read_b128 v[156:159], v142 offset:16384
	ds_read_b128 v[160:163], v142 offset:17408
	ds_read_b128 v[164:167], v142 offset:18432
	ds_read_b128 v[168:171], v142 offset:19456
	ds_read_b128 v[172:175], v142 offset:20480
	ds_read_b128 v[176:179], v142 offset:21504
	ds_read_b128 v[180:183], v142 offset:22528
	ds_read_b128 v[184:187], v142 offset:23552
	global_load_lds_dwordx4 v[212:213], off
	v_lshl_add_u64 v[214:215], s[26:27], 0, v[128:129]
	s_mov_b32 m0, s60
	s_nop 0
	global_load_lds_dwordx4 v[214:215], off
	s_barrier
	s_waitcnt lgkmcnt(0)
	s_setprio 1
	s_waitcnt lgkmcnt(0)
	v_mfma_f32_16x16x32_bf16 v[60:63], v[136:139], v[156:159], v[60:63]
	v_mfma_f32_16x16x32_bf16 v[56:59], v[148:151], v[156:159], v[56:59]
	v_mfma_f32_16x16x32_bf16 v[44:47], v[136:139], v[164:167], v[44:47]
	v_mfma_f32_16x16x32_bf16 v[40:43], v[148:151], v[164:167], v[40:43]
	v_mfma_f32_16x16x32_bf16 v[28:31], v[136:139], v[172:175], v[28:31]
	v_mfma_f32_16x16x32_bf16 v[24:27], v[148:151], v[172:175], v[24:27]
	v_mfma_f32_16x16x32_bf16 v[12:15], v[136:139], v[180:183], v[12:15]
	v_mfma_f32_16x16x32_bf16 v[8:11], v[148:151], v[180:183], v[8:11]
	v_mfma_f32_16x16x32_bf16 v[60:63], v[144:147], v[160:163], v[60:63]
	v_mfma_f32_16x16x32_bf16 v[56:59], v[152:155], v[160:163], v[56:59]
	v_mfma_f32_16x16x32_bf16 v[44:47], v[144:147], v[168:171], v[44:47]
	v_mfma_f32_16x16x32_bf16 v[40:43], v[152:155], v[168:171], v[40:43]
	v_mfma_f32_16x16x32_bf16 v[28:31], v[144:147], v[176:179], v[28:31]
	v_mfma_f32_16x16x32_bf16 v[24:27], v[152:155], v[176:179], v[24:27]
	v_mfma_f32_16x16x32_bf16 v[12:15], v[144:147], v[184:187], v[12:15]
	v_mfma_f32_16x16x32_bf16 v[8:11], v[152:155], v[184:187], v[8:11]
	s_setprio 0
	s_barrier
	s_add_u32 vcc_lo, s24, 0x80000
	s_addc_u32 vcc_hi, s25, 0
	s_add_i32 s28, s72, s47
	v_lshl_add_u64 v[136:137], vcc, 0, v[130:131]
	s_mov_b32 m0, s28
	s_nop 0
	global_load_lds_dwordx4 v[136:137], off
	v_lshl_add_u64 v[136:137], vcc, 0, v[128:129]
	s_add_i32 m0, s28, 0x2000
	s_nop 0
	global_load_lds_dwordx4 v[136:137], off
	s_waitcnt vmcnt(6)
	s_barrier
	s_setprio 1
	v_mfma_f32_16x16x32_bf16 v[52:55], v[188:191], v[156:159], v[52:55]
	v_mfma_f32_16x16x32_bf16 v[48:51], v[196:199], v[156:159], v[48:51]
	v_mfma_f32_16x16x32_bf16 v[36:39], v[188:191], v[164:167], v[36:39]
	v_mfma_f32_16x16x32_bf16 v[32:35], v[196:199], v[164:167], v[32:35]
	v_mfma_f32_16x16x32_bf16 v[20:23], v[188:191], v[172:175], v[20:23]
	v_mfma_f32_16x16x32_bf16 v[16:19], v[196:199], v[172:175], v[16:19]
	v_mfma_f32_16x16x32_bf16 v[4:7], v[188:191], v[180:183], v[4:7]
	v_mfma_f32_16x16x32_bf16 v[0:3], v[196:199], v[180:183], v[0:3]
	v_mfma_f32_16x16x32_bf16 v[52:55], v[192:195], v[160:163], v[52:55]
	v_mfma_f32_16x16x32_bf16 v[48:51], v[200:203], v[160:163], v[48:51]
	v_mfma_f32_16x16x32_bf16 v[36:39], v[192:195], v[168:171], v[36:39]
	v_mfma_f32_16x16x32_bf16 v[32:35], v[200:203], v[168:171], v[32:35]
	v_mfma_f32_16x16x32_bf16 v[20:23], v[192:195], v[176:179], v[20:23]
	v_mfma_f32_16x16x32_bf16 v[16:19], v[200:203], v[176:179], v[16:19]
	v_mfma_f32_16x16x32_bf16 v[4:7], v[192:195], v[184:187], v[4:7]
	v_mfma_f32_16x16x32_bf16 v[0:3], v[200:203], v[184:187], v[0:3]
	s_setprio 0
	s_add_i32 s28, 0, 0x18000
	v_add_u32_e32 v143, s28, v141
	s_barrier
	ds_read_b128 v[136:139], v143
	ds_read_b128 v[144:147], v143 offset:1024
	ds_read_b128 v[148:151], v143 offset:2048
	ds_read_b128 v[152:155], v143 offset:3072
	s_add_u32 s26, s26, 0x80000
	s_addc_u32 s27, s27, 0
	s_mov_b32 m0, s61
	v_lshl_add_u64 v[188:189], s[26:27], 0, v[130:131]
	ds_read_b128 v[156:159], v142 offset:32768
	ds_read_b128 v[160:163], v142 offset:33792
	ds_read_b128 v[164:167], v142 offset:34816
	ds_read_b128 v[168:171], v142 offset:35840
	ds_read_b128 v[172:175], v142 offset:36864
	ds_read_b128 v[176:179], v142 offset:37888
	ds_read_b128 v[180:183], v142 offset:38912
	ds_read_b128 v[184:187], v142 offset:39936
	global_load_lds_dwordx4 v[188:189], off
	v_lshl_add_u64 v[188:189], s[26:27], 0, v[128:129]
	s_mov_b32 m0, s62
	s_nop 0
	global_load_lds_dwordx4 v[188:189], off
	s_waitcnt lgkmcnt(8)
	s_barrier
	s_waitcnt lgkmcnt(0)
	s_setprio 1
	s_waitcnt lgkmcnt(0)
	v_mfma_f32_16x16x32_bf16 v[124:127], v[136:139], v[156:159], v[124:127]
	v_mfma_f32_16x16x32_bf16 v[120:123], v[148:151], v[156:159], v[120:123]
	v_mfma_f32_16x16x32_bf16 v[108:111], v[136:139], v[164:167], v[108:111]
	v_mfma_f32_16x16x32_bf16 v[104:107], v[148:151], v[164:167], v[104:107]
	v_mfma_f32_16x16x32_bf16 v[92:95], v[136:139], v[172:175], v[92:95]
	v_mfma_f32_16x16x32_bf16 v[88:91], v[148:151], v[172:175], v[88:91]
	v_mfma_f32_16x16x32_bf16 v[76:79], v[136:139], v[180:183], v[76:79]
	v_mfma_f32_16x16x32_bf16 v[72:75], v[148:151], v[180:183], v[72:75]
	v_mfma_f32_16x16x32_bf16 v[124:127], v[144:147], v[160:163], v[124:127]
	v_mfma_f32_16x16x32_bf16 v[120:123], v[152:155], v[160:163], v[120:123]
	v_mfma_f32_16x16x32_bf16 v[108:111], v[144:147], v[168:171], v[108:111]
	v_mfma_f32_16x16x32_bf16 v[104:107], v[152:155], v[168:171], v[104:107]
	v_mfma_f32_16x16x32_bf16 v[92:95], v[144:147], v[176:179], v[92:95]
	v_mfma_f32_16x16x32_bf16 v[88:91], v[152:155], v[176:179], v[88:91]
	v_mfma_f32_16x16x32_bf16 v[76:79], v[144:147], v[184:187], v[76:79]
	v_mfma_f32_16x16x32_bf16 v[72:75], v[152:155], v[184:187], v[72:75]
	s_setprio 0
	s_barrier
	s_add_i32 s26, 0, 0x1c000
	s_add_i32 s27, s28, s47
	v_add_u32_e32 v143, s26, v141
	v_lshl_add_u64 v[204:205], v[204:205], 0, s[68:69]
	s_mov_b32 m0, s27
	ds_read_b128 v[188:191], v143
	ds_read_b128 v[192:195], v143 offset:1024
	ds_read_b128 v[196:199], v143 offset:2048
	ds_read_b128 v[200:203], v143 offset:3072
	global_load_lds_dwordx4 v[204:205], off
	v_lshl_add_u64 v[204:205], v[206:207], 0, s[68:69]
	s_add_i32 m0, s27, 0x2000
	s_nop 0
	global_load_lds_dwordx4 v[204:205], off
	s_barrier
	s_waitcnt lgkmcnt(0)
	s_setprio 1
	s_waitcnt lgkmcnt(0)
	v_mfma_f32_16x16x32_bf16 v[116:119], v[188:191], v[156:159], v[116:119]
	v_mfma_f32_16x16x32_bf16 v[112:115], v[196:199], v[156:159], v[112:115]
	v_mfma_f32_16x16x32_bf16 v[100:103], v[188:191], v[164:167], v[100:103]
	v_mfma_f32_16x16x32_bf16 v[96:99], v[196:199], v[164:167], v[96:99]
	v_mfma_f32_16x16x32_bf16 v[84:87], v[188:191], v[172:175], v[84:87]
	v_mfma_f32_16x16x32_bf16 v[80:83], v[196:199], v[172:175], v[80:83]
	v_mfma_f32_16x16x32_bf16 v[68:71], v[188:191], v[180:183], v[68:71]
	v_mfma_f32_16x16x32_bf16 v[64:67], v[196:199], v[180:183], v[64:67]
	v_mfma_f32_16x16x32_bf16 v[116:119], v[192:195], v[160:163], v[116:119]
	v_mfma_f32_16x16x32_bf16 v[112:115], v[200:203], v[160:163], v[112:115]
	v_mfma_f32_16x16x32_bf16 v[100:103], v[192:195], v[168:171], v[100:103]
	v_mfma_f32_16x16x32_bf16 v[96:99], v[200:203], v[168:171], v[96:99]
	v_mfma_f32_16x16x32_bf16 v[84:87], v[192:195], v[176:179], v[84:87]
	v_mfma_f32_16x16x32_bf16 v[80:83], v[200:203], v[176:179], v[80:83]
	v_mfma_f32_16x16x32_bf16 v[68:71], v[192:195], v[184:187], v[68:71]
	v_mfma_f32_16x16x32_bf16 v[64:67], v[200:203], v[184:187], v[64:67]
	s_setprio 0
	s_mov_b32 m0, s63
	v_lshl_add_u64 v[204:205], v[212:213], 0, s[68:69]
	s_barrier
	ds_read_b128 v[156:159], v142 offset:49152
	ds_read_b128 v[160:163], v142 offset:50176
	ds_read_b128 v[164:167], v142 offset:51200
	ds_read_b128 v[168:171], v142 offset:52224
	ds_read_b128 v[172:175], v142 offset:53248
	ds_read_b128 v[176:179], v142 offset:54272
	ds_read_b128 v[180:183], v142 offset:55296
	ds_read_b128 v[184:187], v142 offset:56320
	global_load_lds_dwordx4 v[204:205], off
	v_lshl_add_u64 v[204:205], v[214:215], 0, s[68:69]
	s_mov_b32 m0, s74
	s_nop 0
	global_load_lds_dwordx4 v[204:205], off
	s_barrier
	s_waitcnt lgkmcnt(0)
	s_setprio 1
	s_waitcnt lgkmcnt(0)
	v_mfma_f32_16x16x32_bf16 v[60:63], v[136:139], v[156:159], v[60:63]
	v_mfma_f32_16x16x32_bf16 v[56:59], v[148:151], v[156:159], v[56:59]
	v_mfma_f32_16x16x32_bf16 v[44:47], v[136:139], v[164:167], v[44:47]
	v_mfma_f32_16x16x32_bf16 v[40:43], v[148:151], v[164:167], v[40:43]
	v_mfma_f32_16x16x32_bf16 v[28:31], v[136:139], v[172:175], v[28:31]
	v_mfma_f32_16x16x32_bf16 v[24:27], v[148:151], v[172:175], v[24:27]
	v_mfma_f32_16x16x32_bf16 v[12:15], v[136:139], v[180:183], v[12:15]
	v_mfma_f32_16x16x32_bf16 v[8:11], v[148:151], v[180:183], v[8:11]
	v_mfma_f32_16x16x32_bf16 v[60:63], v[144:147], v[160:163], v[60:63]
	v_mfma_f32_16x16x32_bf16 v[56:59], v[152:155], v[160:163], v[56:59]
	v_mfma_f32_16x16x32_bf16 v[44:47], v[144:147], v[168:171], v[44:47]
	v_mfma_f32_16x16x32_bf16 v[40:43], v[152:155], v[168:171], v[40:43]
	v_mfma_f32_16x16x32_bf16 v[28:31], v[144:147], v[176:179], v[28:31]
	v_mfma_f32_16x16x32_bf16 v[24:27], v[152:155], v[176:179], v[24:27]
	v_mfma_f32_16x16x32_bf16 v[12:15], v[144:147], v[184:187], v[12:15]
	v_mfma_f32_16x16x32_bf16 v[8:11], v[152:155], v[184:187], v[8:11]
	s_setprio 0
	s_barrier
	s_add_u32 s24, s24, 0x80080
	s_addc_u32 s25, s25, 0
	s_add_i32 s26, s26, s47
	v_lshl_add_u64 v[136:137], s[24:25], 0, v[130:131]
	s_mov_b32 m0, s26
	s_nop 0
	global_load_lds_dwordx4 v[136:137], off
	v_lshl_add_u64 v[136:137], s[24:25], 0, v[128:129]
	s_add_i32 m0, s26, 0x2000
	s_nop 0
	global_load_lds_dwordx4 v[136:137], off
	s_waitcnt vmcnt(6)
	s_barrier
	s_setprio 1
	v_mfma_f32_16x16x32_bf16 v[52:55], v[188:191], v[156:159], v[52:55]
	v_mfma_f32_16x16x32_bf16 v[48:51], v[196:199], v[156:159], v[48:51]
	v_mfma_f32_16x16x32_bf16 v[36:39], v[188:191], v[164:167], v[36:39]
	v_mfma_f32_16x16x32_bf16 v[32:35], v[196:199], v[164:167], v[32:35]
	v_mfma_f32_16x16x32_bf16 v[20:23], v[188:191], v[172:175], v[20:23]
	v_mfma_f32_16x16x32_bf16 v[16:19], v[196:199], v[172:175], v[16:19]
	v_mfma_f32_16x16x32_bf16 v[4:7], v[188:191], v[180:183], v[4:7]
	v_mfma_f32_16x16x32_bf16 v[0:3], v[196:199], v[180:183], v[0:3]
	v_mfma_f32_16x16x32_bf16 v[52:55], v[192:195], v[160:163], v[52:55]
	v_mfma_f32_16x16x32_bf16 v[48:51], v[200:203], v[160:163], v[48:51]
	v_mfma_f32_16x16x32_bf16 v[36:39], v[192:195], v[168:171], v[36:39]
	v_mfma_f32_16x16x32_bf16 v[32:35], v[200:203], v[168:171], v[32:35]
	v_mfma_f32_16x16x32_bf16 v[20:23], v[192:195], v[176:179], v[20:23]
	v_mfma_f32_16x16x32_bf16 v[16:19], v[200:203], v[176:179], v[16:19]
	v_mfma_f32_16x16x32_bf16 v[4:7], v[192:195], v[184:187], v[4:7]
	v_mfma_f32_16x16x32_bf16 v[0:3], v[200:203], v[184:187], v[0:3]
	s_setprio 0
	s_add_i32 s65, s65, 2
	s_add_u32 s22, s22, 0x100
	s_addc_u32 s23, s23, 0
	s_add_u32 s85, s85, 0x100
	s_addc_u32 s64, s64, 0
	s_cmp_gt_u32 s65, 29
	s_barrier
	s_cbranch_scc0 .LBB0_529
	v_lshl_add_u32 v138, s20, 8, v140
	v_ashrrev_i32_e32 v139, 31, v138
	v_lshl_add_u64 v[146:147], v[138:139], 2, s[6:7]
	global_load_dword v222, v[146:147], off
	global_load_dword v223, v[146:147], off offset:64
	global_load_dword v224, v[146:147], off offset:128
	global_load_dword v225, v[146:147], off offset:192
	global_load_dword v226, v[146:147], off offset:512
	global_load_dword v227, v[146:147], off offset:576
	global_load_dword v228, v[146:147], off offset:640
	global_load_dword v229, v[146:147], off offset:704
	s_lshl_b32 s20, s21, 8
	s_ashr_i32 s21, s20, 31
	v_mov_b64_e32 v[136:137], s[4:5]
	v_mad_i64_i32 v[144:145], s[22:23], v138, s48, v[136:137]
	s_lshl_b64 s[20:21], s[20:21], 1
	v_lshl_add_u64 v[144:145], v[144:145], 0, s[20:21]
	v_lshl_add_u64 v[144:145], v[144:145], 0, s[50:51]
	v_lshl_add_u64 v[144:145], v[144:145], 0, v[208:209]
	s_and_b64 vcc, exec, s[2:3]
	s_mov_b64 s[24:25], s[18:19]
	s_waitcnt vmcnt(0)
	v_mov_b32_e32 v146, v222
	v_pk_mul_f32 v[126:127], v[126:127], v[146:147] op_sel_hi:[1,0]
	v_pk_mul_f32 v[124:125], v[124:125], v[146:147] op_sel_hi:[1,0]
	v_pk_mul_f32 v[148:149], v[122:123], v[146:147] op_sel_hi:[1,0]
	v_pk_mul_f32 v[122:123], v[120:121], v[146:147] op_sel_hi:[1,0]
	v_cvt_pk_bf16_f32 v120, v124, v125
	v_cvt_pk_bf16_f32 v121, v126, v127
	v_cvt_pk_bf16_f32 v122, v122, v123
	v_cvt_pk_bf16_f32 v123, v148, v149
	global_store_dwordx4 v[144:145], v[120:123], off
	v_pk_mul_f32 v[118:119], v[118:119], v[146:147] op_sel_hi:[1,0]
	v_pk_mul_f32 v[116:117], v[116:117], v[146:147] op_sel_hi:[1,0]
	v_pk_mul_f32 v[120:121], v[114:115], v[146:147] op_sel_hi:[1,0]
	v_pk_mul_f32 v[114:115], v[112:113], v[146:147] op_sel_hi:[1,0]
	v_cvt_pk_bf16_f32 v112, v116, v117
	v_cvt_pk_bf16_f32 v113, v118, v119
	v_cvt_pk_bf16_f32 v114, v114, v115
	v_cvt_pk_bf16_f32 v115, v120, v121
	global_store_dwordx4 v[144:145], v[112:115], off offset:256
	s_nop 1
	v_or_b32_e32 v112, 16, v138
	v_ashrrev_i32_e32 v113, 31, v112
	v_mad_i64_i32 v[114:115], s[22:23], v112, s48, v[136:137]
	v_lshl_add_u64 v[112:113], v[112:113], 2, s[6:7]
	v_lshl_add_u64 v[114:115], v[114:115], 0, s[20:21]
	v_lshl_add_u64 v[114:115], v[114:115], 0, s[50:51]
	v_lshl_add_u64 v[114:115], v[114:115], 0, v[208:209]
	v_mov_b32_e32 v112, v223
	v_pk_mul_f32 v[110:111], v[110:111], v[112:113] op_sel_hi:[1,0]
	v_pk_mul_f32 v[108:109], v[108:109], v[112:113] op_sel_hi:[1,0]
	v_pk_mul_f32 v[116:117], v[106:107], v[112:113] op_sel_hi:[1,0]
	v_pk_mul_f32 v[106:107], v[104:105], v[112:113] op_sel_hi:[1,0]
	v_cvt_pk_bf16_f32 v104, v108, v109
	v_cvt_pk_bf16_f32 v105, v110, v111
	v_cvt_pk_bf16_f32 v106, v106, v107
	v_cvt_pk_bf16_f32 v107, v116, v117
	global_store_dwordx4 v[114:115], v[104:107], off
	v_pk_mul_f32 v[102:103], v[102:103], v[112:113] op_sel_hi:[1,0]
	v_pk_mul_f32 v[100:101], v[100:101], v[112:113] op_sel_hi:[1,0]
	v_pk_mul_f32 v[104:105], v[98:99], v[112:113] op_sel_hi:[1,0]
	v_pk_mul_f32 v[98:99], v[96:97], v[112:113] op_sel_hi:[1,0]
	v_cvt_pk_bf16_f32 v96, v100, v101
	v_cvt_pk_bf16_f32 v97, v102, v103
	v_cvt_pk_bf16_f32 v98, v98, v99
	v_cvt_pk_bf16_f32 v99, v104, v105
	global_store_dwordx4 v[114:115], v[96:99], off offset:256
	s_nop 1
	v_or_b32_e32 v96, 32, v138
	v_ashrrev_i32_e32 v97, 31, v96
	v_mad_i64_i32 v[98:99], s[22:23], v96, s48, v[136:137]
	v_lshl_add_u64 v[96:97], v[96:97], 2, s[6:7]
	v_lshl_add_u64 v[98:99], v[98:99], 0, s[20:21]
	v_lshl_add_u64 v[98:99], v[98:99], 0, s[50:51]
	v_lshl_add_u64 v[98:99], v[98:99], 0, v[208:209]
	v_mov_b32_e32 v96, v224
	v_pk_mul_f32 v[94:95], v[94:95], v[96:97] op_sel_hi:[1,0]
	v_pk_mul_f32 v[92:93], v[92:93], v[96:97] op_sel_hi:[1,0]
	v_pk_mul_f32 v[100:101], v[90:91], v[96:97] op_sel_hi:[1,0]
	v_pk_mul_f32 v[90:91], v[88:89], v[96:97] op_sel_hi:[1,0]
	v_cvt_pk_bf16_f32 v88, v92, v93
	v_cvt_pk_bf16_f32 v89, v94, v95
	v_cvt_pk_bf16_f32 v90, v90, v91
	v_cvt_pk_bf16_f32 v91, v100, v101
	global_store_dwordx4 v[98:99], v[88:91], off
	v_pk_mul_f32 v[86:87], v[86:87], v[96:97] op_sel_hi:[1,0]
	v_pk_mul_f32 v[84:85], v[84:85], v[96:97] op_sel_hi:[1,0]
	v_pk_mul_f32 v[88:89], v[82:83], v[96:97] op_sel_hi:[1,0]
	v_pk_mul_f32 v[82:83], v[80:81], v[96:97] op_sel_hi:[1,0]
	v_cvt_pk_bf16_f32 v80, v84, v85
	v_cvt_pk_bf16_f32 v81, v86, v87
	v_cvt_pk_bf16_f32 v82, v82, v83
	v_cvt_pk_bf16_f32 v83, v88, v89
	global_store_dwordx4 v[98:99], v[80:83], off offset:256
	s_nop 1
	v_or_b32_e32 v80, 48, v138
	v_ashrrev_i32_e32 v81, 31, v80
	v_mad_i64_i32 v[82:83], s[22:23], v80, s48, v[136:137]
	v_lshl_add_u64 v[80:81], v[80:81], 2, s[6:7]
	v_lshl_add_u64 v[82:83], v[82:83], 0, s[20:21]
	v_lshl_add_u64 v[82:83], v[82:83], 0, s[50:51]
	v_lshl_add_u64 v[82:83], v[82:83], 0, v[208:209]
	v_mov_b32_e32 v80, v225
	v_pk_mul_f32 v[78:79], v[78:79], v[80:81] op_sel_hi:[1,0]
	v_pk_mul_f32 v[76:77], v[76:77], v[80:81] op_sel_hi:[1,0]
	v_pk_mul_f32 v[84:85], v[74:75], v[80:81] op_sel_hi:[1,0]
	v_pk_mul_f32 v[74:75], v[72:73], v[80:81] op_sel_hi:[1,0]
	v_cvt_pk_bf16_f32 v72, v76, v77
	v_cvt_pk_bf16_f32 v73, v78, v79
	v_cvt_pk_bf16_f32 v74, v74, v75
	v_cvt_pk_bf16_f32 v75, v84, v85
	global_store_dwordx4 v[82:83], v[72:75], off
	v_pk_mul_f32 v[70:71], v[70:71], v[80:81] op_sel_hi:[1,0]
	v_pk_mul_f32 v[68:69], v[68:69], v[80:81] op_sel_hi:[1,0]
	v_pk_mul_f32 v[72:73], v[66:67], v[80:81] op_sel_hi:[1,0]
	v_pk_mul_f32 v[66:67], v[64:65], v[80:81] op_sel_hi:[1,0]
	v_cvt_pk_bf16_f32 v64, v68, v69
	v_cvt_pk_bf16_f32 v65, v70, v71
	v_cvt_pk_bf16_f32 v66, v66, v67
	v_cvt_pk_bf16_f32 v67, v72, v73
	global_store_dwordx4 v[82:83], v[64:67], off offset:256
	s_nop 1
	v_add_u32_e32 v64, 0x80, v138
	v_ashrrev_i32_e32 v65, 31, v64
	v_mad_i64_i32 v[66:67], s[22:23], v64, s48, v[136:137]
	v_lshl_add_u64 v[64:65], v[64:65], 2, s[6:7]
	v_lshl_add_u64 v[66:67], v[66:67], 0, s[20:21]
	v_lshl_add_u64 v[66:67], v[66:67], 0, s[50:51]
	v_lshl_add_u64 v[66:67], v[66:67], 0, v[208:209]
	v_mov_b32_e32 v64, v226
	v_pk_mul_f32 v[62:63], v[62:63], v[64:65] op_sel_hi:[1,0]
	v_pk_mul_f32 v[60:61], v[60:61], v[64:65] op_sel_hi:[1,0]
	v_pk_mul_f32 v[68:69], v[58:59], v[64:65] op_sel_hi:[1,0]
	v_pk_mul_f32 v[58:59], v[56:57], v[64:65] op_sel_hi:[1,0]
	v_cvt_pk_bf16_f32 v56, v60, v61
	v_cvt_pk_bf16_f32 v57, v62, v63
	v_cvt_pk_bf16_f32 v58, v58, v59
	v_cvt_pk_bf16_f32 v59, v68, v69
	global_store_dwordx4 v[66:67], v[56:59], off
	v_pk_mul_f32 v[54:55], v[54:55], v[64:65] op_sel_hi:[1,0]
	v_pk_mul_f32 v[52:53], v[52:53], v[64:65] op_sel_hi:[1,0]
	v_pk_mul_f32 v[56:57], v[50:51], v[64:65] op_sel_hi:[1,0]
	v_pk_mul_f32 v[50:51], v[48:49], v[64:65] op_sel_hi:[1,0]
	v_cvt_pk_bf16_f32 v48, v52, v53
	v_cvt_pk_bf16_f32 v49, v54, v55
	v_cvt_pk_bf16_f32 v50, v50, v51
	v_cvt_pk_bf16_f32 v51, v56, v57
	global_store_dwordx4 v[66:67], v[48:51], off offset:256
	s_nop 1
	v_add_u32_e32 v48, 0x90, v138
	v_ashrrev_i32_e32 v49, 31, v48
	v_mad_i64_i32 v[50:51], s[22:23], v48, s48, v[136:137]
	v_lshl_add_u64 v[48:49], v[48:49], 2, s[6:7]
	v_lshl_add_u64 v[50:51], v[50:51], 0, s[20:21]
	v_lshl_add_u64 v[50:51], v[50:51], 0, s[50:51]
	v_lshl_add_u64 v[50:51], v[50:51], 0, v[208:209]
	v_mov_b32_e32 v48, v227
	v_pk_mul_f32 v[46:47], v[46:47], v[48:49] op_sel_hi:[1,0]
	v_pk_mul_f32 v[44:45], v[44:45], v[48:49] op_sel_hi:[1,0]
	v_pk_mul_f32 v[52:53], v[42:43], v[48:49] op_sel_hi:[1,0]
	v_pk_mul_f32 v[42:43], v[40:41], v[48:49] op_sel_hi:[1,0]
	v_cvt_pk_bf16_f32 v40, v44, v45
	v_cvt_pk_bf16_f32 v41, v46, v47
	v_cvt_pk_bf16_f32 v42, v42, v43
	v_cvt_pk_bf16_f32 v43, v52, v53
	global_store_dwordx4 v[50:51], v[40:43], off
	v_pk_mul_f32 v[38:39], v[38:39], v[48:49] op_sel_hi:[1,0]
	v_pk_mul_f32 v[36:37], v[36:37], v[48:49] op_sel_hi:[1,0]
	v_pk_mul_f32 v[40:41], v[34:35], v[48:49] op_sel_hi:[1,0]
	v_pk_mul_f32 v[34:35], v[32:33], v[48:49] op_sel_hi:[1,0]
	v_cvt_pk_bf16_f32 v32, v36, v37
	v_cvt_pk_bf16_f32 v33, v38, v39
	v_cvt_pk_bf16_f32 v34, v34, v35
	v_cvt_pk_bf16_f32 v35, v40, v41
	global_store_dwordx4 v[50:51], v[32:35], off offset:256
	s_nop 1
	v_add_u32_e32 v32, 0xa0, v138
	v_ashrrev_i32_e32 v33, 31, v32
	v_mad_i64_i32 v[34:35], s[22:23], v32, s48, v[136:137]
	v_lshl_add_u64 v[32:33], v[32:33], 2, s[6:7]
	v_lshl_add_u64 v[34:35], v[34:35], 0, s[20:21]
	v_lshl_add_u64 v[34:35], v[34:35], 0, s[50:51]
	v_lshl_add_u64 v[34:35], v[34:35], 0, v[208:209]
	v_mov_b32_e32 v32, v228
	v_pk_mul_f32 v[30:31], v[30:31], v[32:33] op_sel_hi:[1,0]
	v_pk_mul_f32 v[28:29], v[28:29], v[32:33] op_sel_hi:[1,0]
	v_pk_mul_f32 v[36:37], v[26:27], v[32:33] op_sel_hi:[1,0]
	v_pk_mul_f32 v[26:27], v[24:25], v[32:33] op_sel_hi:[1,0]
	v_cvt_pk_bf16_f32 v24, v28, v29
	v_cvt_pk_bf16_f32 v25, v30, v31
	v_cvt_pk_bf16_f32 v26, v26, v27
	v_cvt_pk_bf16_f32 v27, v36, v37
	global_store_dwordx4 v[34:35], v[24:27], off
	v_pk_mul_f32 v[22:23], v[22:23], v[32:33] op_sel_hi:[1,0]
	v_pk_mul_f32 v[20:21], v[20:21], v[32:33] op_sel_hi:[1,0]
	v_pk_mul_f32 v[24:25], v[18:19], v[32:33] op_sel_hi:[1,0]
	v_pk_mul_f32 v[18:19], v[16:17], v[32:33] op_sel_hi:[1,0]
	v_cvt_pk_bf16_f32 v16, v20, v21
	v_cvt_pk_bf16_f32 v17, v22, v23
	v_cvt_pk_bf16_f32 v18, v18, v19
	v_cvt_pk_bf16_f32 v19, v24, v25
	global_store_dwordx4 v[34:35], v[16:19], off offset:256
	s_nop 1
	v_add_u32_e32 v16, 0xb0, v138
	v_ashrrev_i32_e32 v17, 31, v16
	v_lshl_add_u64 v[18:19], v[16:17], 2, s[6:7]
	v_mad_i64_i32 v[16:17], s[22:23], v16, s48, v[136:137]
	v_lshl_add_u64 v[16:17], v[16:17], 0, s[20:21]
	v_lshl_add_u64 v[16:17], v[16:17], 0, s[50:51]
	v_lshl_add_u64 v[16:17], v[16:17], 0, v[208:209]
	s_mov_b32 s21, s8
	s_mov_b32 s20, s10
	s_mov_b64 s[22:23], s[16:17]
	v_mov_b32_e32 v18, v229
	v_pk_mul_f32 v[14:15], v[14:15], v[18:19] op_sel_hi:[1,0]
	v_pk_mul_f32 v[12:13], v[12:13], v[18:19] op_sel_hi:[1,0]
	v_pk_mul_f32 v[20:21], v[10:11], v[18:19] op_sel_hi:[1,0]
	v_pk_mul_f32 v[10:11], v[8:9], v[18:19] op_sel_hi:[1,0]
	v_cvt_pk_bf16_f32 v8, v12, v13
	v_cvt_pk_bf16_f32 v9, v14, v15
	v_cvt_pk_bf16_f32 v10, v10, v11
	v_cvt_pk_bf16_f32 v11, v20, v21
	global_store_dwordx4 v[16:17], v[8:11], off
	v_pk_mul_f32 v[6:7], v[6:7], v[18:19] op_sel_hi:[1,0]
	v_pk_mul_f32 v[4:5], v[4:5], v[18:19] op_sel_hi:[1,0]
	v_pk_mul_f32 v[8:9], v[2:3], v[18:19] op_sel_hi:[1,0]
	v_pk_mul_f32 v[2:3], v[0:1], v[18:19] op_sel_hi:[1,0]
	v_cvt_pk_bf16_f32 v0, v4, v5
	v_cvt_pk_bf16_f32 v1, v6, v7
	v_cvt_pk_bf16_f32 v2, v2, v3
	v_cvt_pk_bf16_f32 v3, v8, v9
	global_store_dwordx4 v[16:17], v[0:3], off offset:256
	s_cbranch_vccz .LBB0_526
	s_waitcnt vmcnt(0)
	s_cmpk_gt_u32 s40, 0xff
	s_mov_b64 s[74:75], 0x2000
	s_cbranch_scc1 .LBB0_533
	s_barrier

.LBB0_592:
	s_or_b64 exec, exec, s[6:7]
	s_waitcnt lgkmcnt(0)
	s_barrier
	ds_read_b32 v84, v144
	ds_read_u16 v244, v164
	ds_read_u16 v245, v166
	ds_read_u16 v246, v168
	ds_read_u16 v247, v170
	ds_read_b32 v85, v146
	ds_read_b32 v91, v149
	ds_read_b32 v86, v150
	ds_read_b32 v117, v151
	ds_read_b32 v87, v152
	ds_read_b32 v119, v153
	ds_read_b32 v90, v154
	ds_read_b32 v243, v155
	v_add_u32_e32 v88, s30, v111
	v_ashrrev_i32_e32 v89, 31, v88
	v_lshlrev_b64 v[88:89], 12, v[88:89]
	s_add_i32 s26, s26, 1
	v_lshl_add_u64 v[88:89], v[126:127], 0, v[88:89]
	s_waitcnt lgkmcnt(8)
	v_lshlrev_b32_e32 v244, 16, v244
	v_lshlrev_b32_e32 v245, 16, v245
	v_lshlrev_b32_e32 v246, 16, v246
	v_lshlrev_b32_e32 v247, 16, v247
	v_mul_f32_e32 v248, 0x3d372713, v244
	v_mul_f32_e32 v249, 0x3d372713, v245
	v_mul_f32_e32 v250, 0x3d372713, v246
	v_mul_f32_e32 v251, 0x3d372713, v247
	v_mul_f32_e32 v248, v248, v244
	v_mul_f32_e32 v249, v249, v245
	v_mul_f32_e32 v250, v250, v246
	v_mul_f32_e32 v251, v251, v247
	v_fma_f32 v248, v248, v244, v244
	v_fma_f32 v249, v249, v245, v245
	v_fma_f32 v250, v250, v246, v246
	v_fma_f32 v251, v251, v247, v247
	v_mul_f32_e32 v248, 0x3fcc422a, v248
	v_mul_f32_e32 v249, 0x3fcc422a, v249
	v_mul_f32_e32 v250, 0x3fcc422a, v250
	v_mul_f32_e32 v251, 0x3fcc422a, v251
	v_mul_f32_e32 v248, 0xbfb8aa3b, v248
	v_mul_f32_e32 v249, 0xbfb8aa3b, v249
	v_mul_f32_e32 v250, 0xbfb8aa3b, v250
	v_mul_f32_e32 v251, 0xbfb8aa3b, v251
	v_exp_f32_e32 v248, v248
	v_exp_f32_e32 v249, v249
	v_exp_f32_e32 v250, v250
	v_exp_f32_e32 v251, v251
	v_add_f32_e32 v248, 1.0, v248
	v_add_f32_e32 v249, 1.0, v249
	v_add_f32_e32 v250, 1.0, v250
	v_add_f32_e32 v251, 1.0, v251
	v_rcp_f32_e32 v248, v248
	v_rcp_f32_e32 v249, v249
	v_rcp_f32_e32 v250, v250
	v_rcp_f32_e32 v251, v251
	v_mul_f32_e32 v244, v248, v244
	v_mul_f32_e32 v245, v249, v245
	v_mul_f32_e32 v246, v250, v246
	v_mul_f32_e32 v247, v251, v247
	s_waitcnt lgkmcnt(0)
	v_fmac_f32_e32 v91, v84, v85
	v_mul_f32_e32 v248, v91, v244
	v_bfe_u32 v244, v248, 16, 1
	v_add3_u32 v248, v248, v244, s82
	ds_write_b16_d16_hi v165, v248
	v_fmac_f32_e32 v117, v91, v86
	v_mul_f32_e32 v249, v117, v245
	v_bfe_u32 v245, v249, 16, 1
	v_add3_u32 v249, v249, v245, s82
	ds_write_b16_d16_hi v167, v249
	v_fmac_f32_e32 v119, v117, v87
	v_mul_f32_e32 v250, v119, v246
	v_bfe_u32 v246, v250, 16, 1
	v_add3_u32 v250, v250, v246, s82
	ds_write_b16_d16_hi v169, v250
	v_fmac_f32_e32 v243, v119, v90
	v_mul_f32_e32 v251, v243, v247
	v_bfe_u32 v247, v251, 16, 1
	v_add3_u32 v251, v251, v247, s82
	ds_write_b16_d16_hi v171, v251
	v_mov_b32_e32 v84, v243
	ds_read_u16 v244, v172
	ds_read_u16 v245, v174
	ds_read_u16 v246, v176
	ds_read_u16 v247, v178
	ds_read_b32 v85, v156
	ds_read_b32 v91, v157
	ds_read_b32 v86, v158
	ds_read_b32 v117, v159
	ds_read_b32 v87, v160
	ds_read_b32 v119, v161
	ds_read_b32 v90, v162
	ds_read_b32 v243, v163
	s_waitcnt lgkmcnt(8)
	v_lshlrev_b32_e32 v244, 16, v244
	v_lshlrev_b32_e32 v245, 16, v245
	v_lshlrev_b32_e32 v246, 16, v246
	v_lshlrev_b32_e32 v247, 16, v247
	v_mul_f32_e32 v248, 0x3d372713, v244
	v_mul_f32_e32 v249, 0x3d372713, v245
	v_mul_f32_e32 v250, 0x3d372713, v246
	v_mul_f32_e32 v251, 0x3d372713, v247
	v_mul_f32_e32 v248, v248, v244
	v_mul_f32_e32 v249, v249, v245
	v_mul_f32_e32 v250, v250, v246
	v_mul_f32_e32 v251, v251, v247
	v_fma_f32 v248, v248, v244, v244
	v_fma_f32 v249, v249, v245, v245
	v_fma_f32 v250, v250, v246, v246
	v_fma_f32 v251, v251, v247, v247
	v_mul_f32_e32 v248, 0x3fcc422a, v248
	v_mul_f32_e32 v249, 0x3fcc422a, v249
	v_mul_f32_e32 v250, 0x3fcc422a, v250
	v_mul_f32_e32 v251, 0x3fcc422a, v251
	v_mul_f32_e32 v248, 0xbfb8aa3b, v248
	v_mul_f32_e32 v249, 0xbfb8aa3b, v249
	v_mul_f32_e32 v250, 0xbfb8aa3b, v250
	v_mul_f32_e32 v251, 0xbfb8aa3b, v251
	v_exp_f32_e32 v248, v248
	v_exp_f32_e32 v249, v249
	v_exp_f32_e32 v250, v250
	v_exp_f32_e32 v251, v251
	v_add_f32_e32 v248, 1.0, v248
	v_add_f32_e32 v249, 1.0, v249
	v_add_f32_e32 v250, 1.0, v250
	v_add_f32_e32 v251, 1.0, v251
	v_rcp_f32_e32 v248, v248
	v_rcp_f32_e32 v249, v249
	v_rcp_f32_e32 v250, v250
	v_rcp_f32_e32 v251, v251
	v_mul_f32_e32 v244, v248, v244
	v_mul_f32_e32 v245, v249, v245
	v_mul_f32_e32 v246, v250, v246
	v_mul_f32_e32 v247, v251, v247
	s_waitcnt lgkmcnt(0)
	v_fmac_f32_e32 v91, v84, v85
	v_mul_f32_e32 v248, v91, v244
	v_bfe_u32 v244, v248, 16, 1
	v_add3_u32 v248, v248, v244, s82
	ds_write_b16_d16_hi v173, v248
	v_fmac_f32_e32 v117, v91, v86
	v_mul_f32_e32 v249, v117, v245
	v_bfe_u32 v245, v249, 16, 1
	v_add3_u32 v249, v249, v245, s82
	ds_write_b16_d16_hi v175, v249
	v_fmac_f32_e32 v119, v117, v87
	v_mul_f32_e32 v250, v119, v246
	v_bfe_u32 v246, v250, 16, 1
	v_add3_u32 v250, v250, v246, s82
	ds_write_b16_d16_hi v177, v250
	v_fmac_f32_e32 v243, v119, v90
	v_mul_f32_e32 v251, v243, v247
	v_bfe_u32 v247, v251, 16, 1
	v_add3_u32 v251, v251, v247, s82
	ds_write_b16_d16_hi v179, v251
	s_cmp_lg_u32 s26, 8
	s_waitcnt lgkmcnt(0)
	s_barrier
	ds_read_b128 v[84:87], v145
	s_waitcnt lgkmcnt(0)
	global_store_dwordx4 v[88:89], v[84:87], off
	s_cbranch_scc0 .LBB0_590

.LBB0_852:
	v_cmp_lt_i64_e32 vcc, s[14:15], v[218:219]
	s_add_u32 s14, s40, s8
	s_addc_u32 s15, s41, s9
	s_and_b64 s[16:17], vcc, exec
	s_cselect_b32 s7, s15, s21
	s_cselect_b32 s11, s14, s20
	s_add_u32 s16, s42, s12
	s_addc_u32 s17, s43, s13
	s_and_b64 s[24:25], vcc, exec
	s_cselect_b32 s75, s17, s23
	s_cselect_b32 s78, s16, s22
	s_add_u32 s20, s20, 0x80080
	s_addc_u32 s21, s21, 0
	s_add_u32 s79, s22, 0x100
	v_mov_b32_e32 v0, 0
	s_addc_u32 s64, s23, 0
	s_mov_b32 s65, -2
	v_mov_b32_e32 v1, v0
	v_mov_b32_e32 v2, v0
	v_mov_b32_e32 v3, v0
	v_mov_b32_e32 v4, v0
	v_mov_b32_e32 v5, v0
	v_mov_b32_e32 v6, v0
	v_mov_b32_e32 v7, v0
	v_mov_b32_e32 v12, v0
	v_mov_b32_e32 v13, v0
	v_mov_b32_e32 v14, v0
	v_mov_b32_e32 v15, v0
	v_mov_b32_e32 v20, v0
	v_mov_b32_e32 v21, v0
	v_mov_b32_e32 v22, v0
	v_mov_b32_e32 v23, v0
	v_mov_b32_e32 v28, v0
	v_mov_b32_e32 v29, v0
	v_mov_b32_e32 v30, v0
	v_mov_b32_e32 v31, v0
	v_mov_b32_e32 v36, v0
	v_mov_b32_e32 v37, v0
	v_mov_b32_e32 v38, v0
	v_mov_b32_e32 v39, v0
	v_mov_b32_e32 v44, v0
	v_mov_b32_e32 v45, v0
	v_mov_b32_e32 v46, v0
	v_mov_b32_e32 v47, v0
	v_mov_b32_e32 v52, v0
	v_mov_b32_e32 v53, v0
	v_mov_b32_e32 v54, v0
	v_mov_b32_e32 v55, v0
	v_mov_b32_e32 v8, v0
	v_mov_b32_e32 v9, v0
	v_mov_b32_e32 v10, v0
	v_mov_b32_e32 v11, v0
	v_mov_b32_e32 v16, v0
	v_mov_b32_e32 v17, v0
	v_mov_b32_e32 v18, v0
	v_mov_b32_e32 v19, v0
	v_mov_b32_e32 v24, v0
	v_mov_b32_e32 v25, v0
	v_mov_b32_e32 v26, v0
	v_mov_b32_e32 v27, v0
	v_mov_b32_e32 v32, v0
	v_mov_b32_e32 v33, v0
	v_mov_b32_e32 v34, v0
	v_mov_b32_e32 v35, v0
	v_mov_b32_e32 v40, v0
	v_mov_b32_e32 v41, v0
	v_mov_b32_e32 v42, v0
	v_mov_b32_e32 v43, v0
	v_mov_b32_e32 v48, v0
	v_mov_b32_e32 v49, v0
	v_mov_b32_e32 v50, v0
	v_mov_b32_e32 v51, v0
	v_mov_b32_e32 v56, v0
	v_mov_b32_e32 v57, v0
	v_mov_b32_e32 v58, v0
	v_mov_b32_e32 v59, v0
	v_mov_b32_e32 v60, v0
	v_mov_b32_e32 v61, v0
	v_mov_b32_e32 v62, v0
	v_mov_b32_e32 v63, v0
	v_mov_b32_e32 v64, v0
	v_mov_b32_e32 v65, v0
	v_mov_b32_e32 v66, v0
	v_mov_b32_e32 v67, v0
	v_mov_b32_e32 v68, v0
	v_mov_b32_e32 v69, v0
	v_mov_b32_e32 v70, v0
	v_mov_b32_e32 v71, v0
	v_mov_b32_e32 v76, v0
	v_mov_b32_e32 v77, v0
	v_mov_b32_e32 v78, v0
	v_mov_b32_e32 v79, v0
	v_mov_b32_e32 v84, v0
	v_mov_b32_e32 v85, v0
	v_mov_b32_e32 v86, v0
	v_mov_b32_e32 v87, v0
	v_mov_b32_e32 v92, v0
	v_mov_b32_e32 v93, v0
	v_mov_b32_e32 v94, v0
	v_mov_b32_e32 v95, v0
	v_mov_b32_e32 v100, v0
	v_mov_b32_e32 v101, v0
	v_mov_b32_e32 v102, v0
	v_mov_b32_e32 v103, v0
	v_mov_b32_e32 v112, v0
	v_mov_b32_e32 v113, v0
	v_mov_b32_e32 v114, v0
	v_mov_b32_e32 v115, v0
	v_mov_b32_e32 v116, v0
	v_mov_b32_e32 v117, v0
	v_mov_b32_e32 v118, v0
	v_mov_b32_e32 v119, v0
	v_mov_b32_e32 v72, v0
	v_mov_b32_e32 v73, v0
	v_mov_b32_e32 v74, v0
	v_mov_b32_e32 v75, v0
	v_mov_b32_e32 v80, v0
	v_mov_b32_e32 v81, v0
	v_mov_b32_e32 v82, v0
	v_mov_b32_e32 v83, v0
	v_mov_b32_e32 v88, v0
	v_mov_b32_e32 v89, v0
	v_mov_b32_e32 v90, v0
	v_mov_b32_e32 v91, v0
	v_mov_b32_e32 v96, v0
	v_mov_b32_e32 v97, v0
	v_mov_b32_e32 v98, v0
	v_mov_b32_e32 v99, v0
	v_mov_b32_e32 v104, v0
	v_mov_b32_e32 v105, v0
	v_mov_b32_e32 v106, v0
	v_mov_b32_e32 v107, v0
	v_mov_b32_e32 v108, v0
	v_mov_b32_e32 v109, v0
	v_mov_b32_e32 v110, v0
	v_mov_b32_e32 v111, v0
	v_mov_b32_e32 v120, v0
	v_mov_b32_e32 v121, v0
	v_mov_b32_e32 v122, v0
	v_mov_b32_e32 v123, v0
	v_mov_b32_e32 v124, v0
	v_mov_b32_e32 v125, v0
	v_mov_b32_e32 v126, v0
	v_mov_b32_e32 v127, v0

.LBB0_881:
	s_lshl_b32 s21, s60, 5
	v_add_u32_e32 v0, s21, v207
	v_ashrrev_i32_e32 v1, 31, v0
	v_lshlrev_b64 v[0:1], 12, v[0:1]
	s_add_i32 s6, s20, 0
	v_lshl_add_u64 v[40:41], v[80:81], 0, v[0:1]
	s_mov_b32 m0, s6
	s_add_i32 s7, s63, 0
	global_load_dwordx4 v[60:63], v[40:41], off
	global_load_dwordx4 v[56:59], v[40:41], off offset:64
	global_load_dwordx4 v[52:55], v[40:41], off offset:128
	global_load_dwordx4 v[48:51], v[40:41], off offset:192
	global_load_dwordx4 v[0:3], v[40:41], off offset:256
	global_load_dwordx4 v[4:7], v[40:41], off offset:320
	global_load_dwordx4 v[8:11], v[40:41], off offset:384
	global_load_dwordx4 v[12:15], v[40:41], off offset:448
	global_load_dwordx4 v[20:23], v[40:41], off offset:512
	global_load_dwordx4 v[28:31], v[40:41], off offset:576
	global_load_dwordx4 v[36:39], v[40:41], off offset:640
	global_load_dwordx4 v[44:47], v[40:41], off offset:704
	global_load_dwordx4 v[16:19], v[40:41], off offset:768
	global_load_dwordx4 v[24:27], v[40:41], off offset:832
	global_load_dwordx4 v[32:35], v[40:41], off offset:896
	s_nop 0
	global_load_dwordx4 v[40:43], v[40:41], off offset:960
	s_add_i32 s8, s74, 0
	global_load_lds_dwordx4 v[82:83], off
	s_add_i32 m0, s7, 0x2000
	s_add_i32 s9, s75, 0
	global_load_lds_dwordx4 v[84:85], off
	s_add_i32 m0, s8, 0x4000
	v_mov_b32_e32 v144, 0
	global_load_lds_dwordx4 v[86:87], off
	s_add_i32 m0, s9, 0x6000
	s_mov_b32 s12, 0
	global_load_lds_dwordx4 v[88:89], off
	s_add_i32 m0, s6, 0x7800
	v_mov_b32_e32 v76, 0
	global_load_lds_dwordx4 v[90:91], off
	s_add_i32 m0, s7, 0x9800
	v_mov_b32_e32 v77, v144
	global_load_lds_dwordx4 v[92:93], off
	s_add_i32 m0, s8, 0xb800
	v_mov_b32_e32 v78, v144
	global_load_lds_dwordx4 v[94:95], off
	s_add_i32 m0, s9, 0xd800
	v_mov_b32_e32 v79, v144
	global_load_lds_dwordx4 v[96:97], off
	s_add_i32 m0, s6, 0xf000
	s_add_i32 s6, s22, 0
	global_load_lds_dwordx4 v[98:99], off
	s_add_i32 m0, s6, 0xf000
	s_add_i32 s6, s24, 0
	global_load_lds_dwordx4 v[100:101], off
	s_add_i32 m0, s6, 0xf000
	s_add_i32 s6, s26, 0
	global_load_lds_dwordx4 v[102:103], off
	s_add_i32 m0, s6, 0xf000
	s_add_i32 s6, s80, s63
	global_load_lds_dwordx4 v[104:105], off
	s_add_i32 m0, s80, s20
	v_mov_b32_e32 v68, 0
	global_load_lds_dwordx4 v[106:107], off
	s_add_i32 m0, s6, 0x2000
	s_add_i32 s6, s80, s74
	global_load_lds_dwordx4 v[108:109], off
	s_add_i32 m0, s6, 0x4000
	s_add_i32 s6, s80, s75
	global_load_lds_dwordx4 v[110:111], off
	s_add_i32 m0, s6, 0x6000
	s_mov_b64 s[6:7], 0
	global_load_lds_dwordx4 v[112:113], off
	v_mov_b32_e32 v69, v144
	v_mov_b32_e32 v70, v144
	v_mov_b32_e32 v71, v144
	v_mov_b32_e32 v64, 0
	v_mov_b32_e32 v65, v144
	v_mov_b32_e32 v66, v144
	v_mov_b32_e32 v67, v144
.LBB0_882:
	s_cmp_lg_u32 s6, 0x5a000
	s_waitcnt vmcnt(12)
	s_barrier
	s_cselect_b64 s[8:9], -1, 0
	s_mov_b64 s[10:11], -1
	s_and_b64 vcc, exec, s[8:9]
	v_lshl_add_u64 v[142:143], v[128:129], 0, s[6:7]
	v_lshl_add_u64 v[140:141], v[130:131], 0, s[6:7]
	v_lshl_add_u64 v[138:139], v[132:133], 0, s[6:7]
	v_lshl_add_u64 v[136:137], v[134:135], 0, s[6:7]
	s_cbranch_vccz .LBB0_884
	s_mul_i32 s13, s12, 0x7800
	s_add_i32 s10, s13, 0xffff8800
	s_cmp_lg_u32 s12, 0
	s_cselect_b32 s10, s10, 0x1e000
	s_add_i32 s10, s10, 0
	v_lshl_add_u64 v[72:73], v[142:143], 0, s[94:95]
	s_add_i32 m0, s10, s20
	s_add_i32 s11, s10, s63
	global_load_lds_dwordx4 v[72:73], off
	v_lshl_add_u64 v[72:73], v[140:141], 0, s[94:95]
	s_add_i32 m0, s11, 0x2000
	s_add_i32 s11, s10, s74
	global_load_lds_dwordx4 v[72:73], off
	v_lshl_add_u64 v[72:73], v[138:139], 0, s[94:95]
	s_add_i32 m0, s11, 0x4000
	s_add_i32 s10, s10, s75
	global_load_lds_dwordx4 v[72:73], off
	v_lshl_add_u64 v[72:73], v[136:137], 0, s[94:95]
	s_add_i32 m0, s10, 0x6000
	s_mov_b64 s[10:11], 0
	global_load_lds_dwordx4 v[72:73], off

.LBB0_1437:
	s_sext_i32_i8 s85, s6
	s_lshl_b32 s6, s46, 25
	s_and_b32 s6, s6, 0x2000000
	s_add_u32 s6, s2, s6
	s_addc_u32 s7, s3, 0
	s_add_u32 s6, s6, 0x37900000
	s_addc_u32 s7, s7, 0
	s_lshl_b64 s[8:9], s[90:91], 25
	s_add_u32 s8, s2, s8
	s_addc_u32 s9, s3, s9
	s_add_u32 s8, s8, 0x51140000
	s_addc_u32 s9, s9, 0
	s_lshl_b64 s[12:13], s[90:91], 13
	s_waitcnt lgkmcnt(0)
	s_add_u32 s10, s10, s12
	v_lshrrev_b32_e32 v15, 1, v13
	s_addc_u32 s11, s11, s13
	v_and_b32_e32 v15, 24, v15
	s_add_u32 s12, s2, 0x5e250000
	v_and_b32_e32 v243, 15, v13
	v_lshlrev_b32_e32 v16, 1, v15
	v_lshlrev_b32_e32 v13, 2, v13
	s_addc_u32 s13, s3, 0
	v_lshl_or_b32 v16, v243, 6, v16
	s_lshl_b32 s2, s14, 13
	v_and_b32_e32 v13, 32, v13
	v_bitop3_b32 v17, v16, s2, v13 bitop3:0xde
	s_lshl_b32 s2, s15, 5
	s_lshl_b32 s78, s14, 6
	s_and_b32 s14, s2, 0x60
	s_add_i32 m0, s27, 0x18000
	v_lshl_add_u64 v[6:7], v[6:7], 0, s[68:69]
	s_lshl_b32 s2, s14, 7
	s_waitcnt vmcnt(4)
	s_barrier
	global_load_lds_dwordx4 v[6:7], off
	v_lshl_add_u64 v[4:5], v[4:5], 0, s[68:69]
	s_add_i32 m0, s27, 0x1a000
	s_add_i32 s79, s27, 0x8000
	s_add_i32 s90, s27, 0xa000
	v_bitop3_b32 v244, s2, v16, v13 bitop3:0xf6
	global_load_lds_dwordx4 v[4:5], off
	v_lshl_add_u64 v[2:3], v[2:3], 0, s[68:69]
	s_mov_b32 m0, s79
	s_add_u32 s2, s40, 0x80080
	global_load_lds_dwordx4 v[2:3], off
	v_lshl_add_u64 v[0:1], v[0:1], 0, s[68:69]
	s_mov_b32 m0, s90
	s_addc_u32 s3, s41, 0
	global_load_lds_dwordx4 v[0:1], off
	s_add_i32 m0, s27, 0x1c000
	v_lshl_add_u64 v[0:1], s[2:3], 0, v[208:209]
	global_load_lds_dwordx4 v[0:1], off
	v_lshl_add_u64 v[0:1], s[2:3], 0, v[220:221]
	s_add_i32 m0, s27, 0x1e000
	v_or_b32_e32 v245, 0x80, v243
	global_load_lds_dwordx4 v[0:1], off
	v_lshlrev_b32_e32 v0, 15, v8
	v_and_b32_e32 v0, 0xffff0000, v0
	v_lshl_add_u32 v0, v9, 12, v0
	v_and_b32_e32 v1, 1, v8
	v_lshl_or_b32 v0, v1, 6, v0
	v_lshl_add_u32 v222, v10, 1, v0
	v_lshlrev_b32_e32 v0, 15, v11
	v_and_b32_e32 v0, 0xffff0000, v0
	s_waitcnt vmcnt(6)
	v_lshl_add_u32 v0, v12, 12, v0
	v_and_b32_e32 v1, 1, v11
	v_lshl_or_b32 v0, v1, 6, v0
	s_ashr_i32 s91, s47, 31
	v_or_b32_e32 v246, s14, v15
	v_mov_b32_e32 v223, v209
	v_lshl_add_u32 v224, v14, 1, v0
	v_mov_b32_e32 v225, v209
	s_mov_b32 s84, 0
	v_add_u32_e32 v247, 0, v17
	s_barrier
